# rider decode made branch-free scalar code spread after the exponentials of the second key tile; short memory block at the end of the trip; queue of store targets kept in two scalar registers
# baseline (speedup 1.0000x reference)
; DI f32x16 mfma8(v8i a, v8i b, f32x16 c) { return __builtin_amdgcn_mfma_scale_f32_32x32x64_f8f6f4(a, b, c, 0, 0, 0, 0, 0, 0); }
; DI void attn_unit_d8(unsigned char* lds, const AttnArgs& a) {
;     ...
;     auto tile = [&](const unsigned char* Kb, const unsigned char* Kn, v8i& Pa, v8i& Pb, v8i& v0, v8i& v1, const v8i& Qa, const v8i& Qb, const v8i& w0, const v8i& w1) __attribute__((always_inline)) {
;         qk(Kb, 1, s1a, s1b);
;         v0 = rd32(Kb + voff); v1 = rd32(Kb + voff + 32 * A8_PITCH);
;         o0[0] = mfma8(w0, Qa, o0[0]); o1[0] = mfma8(w0, Qb, o1[0]); o0[1] = mfma8(w1, Qa, o0[1]); o1[1] = mfma8(w1, Qb, o1[1]);
;         expsum(s0a, l0); expsum(s0b, l1); pack4(s0a, Pa, 0); pack4(s0b, Pb, 0);
;         qk(Kn, 0, s0a, s0b);
;         expsum(s1a, l0); expsum(s1b, l1); pack4(s1a, Pa, 4); pack4(s1b, Pb, 4);
; #pragma unroll
;         for (int i = 0; i < 8; ++i) { __builtin_amdgcn_sched_group_barrier(0x008, 1, 0); __builtin_amdgcn_sched_group_barrier(0x402, 22, 0); }
;     };
;     for (int t = a.t0; t < a.t1; t += 2) {
;         const int s1 = sb + 1 >= 5 ? sb - 4 : sb + 1, s2 = sb + 2 >= 5 ? sb - 3 : sb + 2, s3 = sb + 3 >= 5 ? sb - 2 : sb + 3, s4 = sb + 4 >= 5 ? sb - 1 : sb + 4;
;         { const int ta = t + 3, tb = t + 4; gload(ta < a.t1 ? ta : a.t1 - 1, kreg0, vreg0); gload(tb < a.t1 ? tb : a.t1 - 1, kreg1, vreg1); }
;         tile(lds + sb * D8_SLOT, lds + s1 * D8_SLOT, PaX, PbX, vX0, vX1, PaY, PbY, vY0, vY1);
;         tile(lds + s1 * D8_SLOT, lds + s2 * D8_SLOT, PaY, PbY, vY0, vY1, PaX, PbX, vX0, vX1);
;         lstore(s3, kreg0, vreg0); lstore(s4, kreg1, vreg1);
;         __syncthreads();
;         sb = s2;
;     }
.LBB0_663:
	s_cmp_gt_i32 s16, 3
	s_cselect_b32 s17, -4, 1
	s_add_i32 s18, s17, s16
	s_mul_i32 s6, s16, 0x2800
	s_cmp_gt_i32 s16, 2
	v_mfma_f32_32x32x64_f8f6f4 v[50:65], v[154:161], v[138:145], v[50:65]
	v_exp_f32_e32 v192, v90
	v_add_u32_e32 v90, s6, v218
	s_cselect_b32 s6, -3, 2
	s_add_i32 s6, s6, s16
	s_cmp_gt_i32 s16, 1
	s_cselect_b32 s19, -2, 3
	s_add_i32 s19, s19, s16
	s_cmp_gt_i32 s16, 0
	s_cselect_b32 s49, -1, 4
	s_min_u32 s54, s46, 64
	s_add_i32 s49, s49, s16
	s_cmp_lt_u32 s46, 61
	s_mul_i32 s17, s6, 0x2800
	s_mov_b32 s16, s6
	s_cselect_b64 s[52:53], -1, 0
	s_lshl_b32 s6, s54, 6
	s_add_i32 s54, s6, 0xc0
	s_add_i32 s55, s6, 0xfffff0c0
	s_and_b64 s[52:53], s[52:53], exec
	v_lshl_add_u64 v[98:99], v[182:183], 0, s[6:7]
	s_cselect_b32 s6, s54, s55
	s_cselect_b32 s53, s21, s48
	s_cselect_b32 s52, s20, s47
	s_min_u32 s56, s46, 63
	v_exp_f32_e32 v198, v82
	v_exp_f32_e32 v199, v83
	v_exp_f32_e32 v196, v84
	v_exp_f32_e32 v197, v85
	v_exp_f32_e32 v200, v86
	v_exp_f32_e32 v201, v87
	v_exp_f32_e32 v194, v88
	v_exp_f32_e32 v195, v89
	ds_read_b128 v[82:85], v90 offset:2560
	ds_read_b128 v[86:89], v90 offset:2576
	global_load_dwordx2 v[202:203], v[98:99], off offset:192
	v_add_u32_e32 v98, s6, v215
	s_cmp_lt_u32 s46, 60
	v_ashrrev_i32_e32 v99, 31, v98
	s_cselect_b64 s[54:55], -1, 0
	s_lshl_b32 s6, s56, 6
	v_lshlrev_b64 v[98:99], 8, v[98:99]
	s_add_i32 s56, s6, 0x100
	s_add_i32 s57, s6, 0xfffff100
	v_lshl_add_u64 v[98:99], s[52:53], 0, v[98:99]
	s_and_b64 s[52:53], s[54:55], exec
	s_cselect_b32 s54, s56, s57
	v_lshl_add_u64 v[220:221], v[98:99], 0, v[178:179]
	v_add_u32_e32 v98, s54, v215
	v_ashrrev_i32_e32 v99, 31, v98
	s_cselect_b32 s53, s21, s48
	s_cselect_b32 s52, s20, s47
	v_lshlrev_b64 v[98:99], 8, v[98:99]
	v_lshl_add_u64 v[100:101], v[182:183], 0, s[6:7]
	v_lshl_add_u64 v[98:99], s[52:53], 0, v[98:99]
	global_load_dwordx2 v[204:205], v[100:101], off offset:256
	v_lshl_add_u64 v[222:223], v[98:99], 0, v[178:179]
	s_waitcnt lgkmcnt(0)
	v_mfma_f32_32x32x64_f8f6f4 v[98:113], v[82:89], v[114:121], 0
	v_exp_f32_e32 v193, v91
	v_exp_f32_e32 v224, v92
	v_exp_f32_e32 v225, v93
	v_exp_f32_e32 v226, v94
	v_exp_f32_e32 v227, v95
	v_exp_f32_e32 v228, v96
	v_exp_f32_e32 v229, v97
	ds_read_b128 v[170:173], v90 offset:5120
	ds_read_b128 v[174:177], v90 offset:5136
	ds_read_b128 v[162:165], v90 offset:7680
	ds_read_b128 v[166:169], v90 offset:7696
	v_pk_add_f32 v[90:91], v[186:187], v[198:199]
	v_pk_add_f32 v[92:93], v[184:185], v[196:197]
	v_pk_add_f32 v[90:91], v[200:201], v[90:91]
	v_pk_add_f32 v[92:93], v[194:195], v[92:93]
	v_pk_add_f32 v[90:91], v[192:193], v[90:91]
	v_pk_add_f32 v[92:93], v[224:225], v[92:93]
	v_exp_f32_e32 v66, v66
	v_exp_f32_e32 v67, v67
	v_exp_f32_e32 v68, v68
	v_exp_f32_e32 v69, v69
	v_exp_f32_e32 v70, v70
	v_exp_f32_e32 v71, v71
	v_exp_f32_e32 v72, v72
	v_pk_add_f32 v[230:231], v[228:229], v[92:93]
	v_pk_add_f32 v[232:233], v[226:227], v[90:91]
	v_mfma_f32_32x32x64_f8f6f4 v[82:97], v[82:89], v[122:129], 0
	v_exp_f32_e32 v73, v73
	v_exp_f32_e32 v74, v74
	v_exp_f32_e32 v75, v75
	v_exp_f32_e32 v76, v76
	v_exp_f32_e32 v77, v77
	v_exp_f32_e32 v78, v78
	v_exp_f32_e32 v79, v79
	v_exp_f32_e32 v80, v80
	v_exp_f32_e32 v81, v81
	v_pk_add_f32 v[186:187], v[190:191], v[66:67]
	v_pk_add_f32 v[188:189], v[188:189], v[68:69]
	s_nop 0
	v_pk_add_f32 v[186:187], v[70:71], v[186:187]
	v_pk_add_f32 v[188:189], v[72:73], v[188:189]
	s_nop 0
	v_cvt_scalef32_pk_fp8_f32 v184, v198, v199, s36
	v_pk_add_f32 v[186:187], v[74:75], v[186:187]
	v_pk_add_f32 v[188:189], v[76:77], v[188:189]
	v_cvt_scalef32_pk_fp8_f32 v185, v200, v201, s36
	v_cvt_scalef32_pk_fp8_f32 v184, v196, v197, s36 op_sel:[0,0,0,1]
	v_pk_add_f32 v[190:191], v[78:79], v[186:187]
	v_pk_add_f32 v[188:189], v[80:81], v[188:189]
	v_mfma_f32_32x32x64_f8f6f4 v[2:17], v[154:161], v[130:137], v[2:17]
	s_nop 0
	s_nop 0
	s_nop 0
	s_nop 0
	s_nop 0
	s_nop 0
	s_mulk_i32 s18, 0x2800
	v_cvt_scalef32_pk_fp8_f32 v186, v192, v193, s36
	v_cvt_scalef32_pk_fp8_f32 v187, v226, v227, s36
	v_cvt_scalef32_pk_fp8_f32 v154, v66, v67, s36
	v_cvt_scalef32_pk_fp8_f32 v155, v70, v71, s36
	v_cvt_scalef32_pk_fp8_f32 v156, v74, v75, s36
	v_cvt_scalef32_pk_fp8_f32 v157, v78, v79, s36
	v_cvt_scalef32_pk_fp8_f32 v185, v194, v195, s36 op_sel:[0,0,0,1]
	v_add_u32_e32 v219, s18, v218
	v_cvt_scalef32_pk_fp8_f32 v186, v224, v225, s36 op_sel:[0,0,0,1]
	v_cvt_scalef32_pk_fp8_f32 v187, v228, v229, s36 op_sel:[0,0,0,1]
	v_cvt_scalef32_pk_fp8_f32 v154, v68, v69, s36 op_sel:[0,0,0,1]
	v_cvt_scalef32_pk_fp8_f32 v155, v72, v73, s36 op_sel:[0,0,0,1]
	v_cvt_scalef32_pk_fp8_f32 v156, v76, v77, s36 op_sel:[0,0,0,1]
	v_cvt_scalef32_pk_fp8_f32 v157, v80, v81, s36 op_sel:[0,0,0,1]
	v_exp_f32_e32 v98, v98
	v_exp_f32_e32 v99, v99
	v_mfma_f32_32x32x64_f8f6f4 v[34:49], v[146:153], v[138:145], v[34:49]
	v_exp_f32_e32 v100, v100
	v_exp_f32_e32 v101, v101
	v_exp_f32_e32 v102, v102
	v_exp_f32_e32 v103, v103
	v_exp_f32_e32 v104, v104
	v_exp_f32_e32 v105, v105
	v_exp_f32_e32 v106, v106
	v_exp_f32_e32 v107, v107
	v_exp_f32_e32 v108, v108
	v_exp_f32_e32 v109, v109
	v_exp_f32_e32 v110, v110
	v_exp_f32_e32 v111, v111
	v_exp_f32_e32 v112, v112
	v_exp_f32_e32 v113, v113
	ds_read_b128 v[192:195], v219
	ds_read_b128 v[196:199], v219 offset:16
	v_pk_add_f32 v[66:67], v[232:233], v[98:99]
	v_pk_add_f32 v[68:69], v[230:231], v[100:101]
	v_pk_add_f32 v[66:67], v[102:103], v[66:67]
	v_pk_add_f32 v[68:69], v[104:105], v[68:69]
	v_pk_add_f32 v[66:67], v[106:107], v[66:67]
	v_pk_add_f32 v[68:69], v[108:109], v[68:69]
	v_pk_add_f32 v[140:141], v[110:111], v[66:67]
	v_pk_add_f32 v[138:139], v[112:113], v[68:69]
	v_mfma_f32_32x32x64_f8f6f4 v[18:33], v[146:153], v[130:137], v[18:33]
	v_exp_f32_e32 v82, v82
	v_exp_f32_e32 v83, v83
	v_exp_f32_e32 v84, v84
	v_exp_f32_e32 v85, v85
	v_exp_f32_e32 v86, v86
	v_exp_f32_e32 v87, v87
	v_exp_f32_e32 v88, v88
	v_exp_f32_e32 v89, v89
	v_exp_f32_e32 v90, v90
	v_exp_f32_e32 v91, v91
	v_exp_f32_e32 v92, v92
	v_exp_f32_e32 v93, v93
	v_exp_f32_e32 v94, v94
	v_exp_f32_e32 v95, v95
	v_exp_f32_e32 v96, v96
	v_exp_f32_e32 v97, v97
	v_pk_add_f32 v[66:67], v[190:191], v[82:83]
	v_pk_add_f32 v[68:69], v[188:189], v[84:85]
	v_pk_add_f32 v[66:67], v[86:87], v[66:67]
	v_pk_add_f32 v[68:69], v[88:89], v[68:69]
	v_pk_add_f32 v[130:131], v[90:91], v[66:67]
	v_pk_add_f32 v[132:133], v[92:93], v[68:69]
	s_waitcnt lgkmcnt(0)
; DI void attn_unit_a8(unsigned char* lds, const AttnArgs& a) {
;     ...
;     auto w_decode = [&](int j, const float*& src, unsigned char*& dst, int& ld, int& n0, int& k0, bool& gu) __attribute__((always_inline)) {
;         const int g = (j >> 2) * 512 + a.wl, e = g / 96, rr = g - e * 96; KParamsPtr kp = kparams();
;         if (rr < 64) { src = kp->w_gu + ((size_t)a.wli * NE + e) * (1024 * 2048); dst = kp->ws + WS_WGU + (size_t)a.wli * SZ_WGU + (size_t)e * 2048 * 1024; ld = 2048; n0 = (rr & 7) * 256; k0 = ((rr >> 3) * 4 + (j & 3)) * 32; gu = true; }
;         else { const int q = rr - 64; src = kp->w_dn + ((size_t)a.wli * NE + e) * (1024 * 1024); dst = kp->ws + WS_WDN + (size_t)a.wli * SZ_WDN + (size_t)e * 1024 * 1024; ld = 1024; n0 = (q & 3) * 256; k0 = ((q >> 2) * 4 + (j & 3)) * 32; gu = false; } };
;     auto w_issue = [&](int j) __attribute__((always_inline)) { const float* src; unsigned char* dst; int ld, n0, k0; bool gu; w_decode(j, src, dst, ld, n0, k0, gu);
;         const float* p = src + (size_t)(k0 + 4 * wid) * ld + n0 + wn4;
;         wq[0] = __builtin_nontemporal_load((const f32x4*)p); wq[1] = __builtin_nontemporal_load((const f32x4*)(p + ld));
;         wq[2] = __builtin_nontemporal_load((const f32x4*)(p + (size_t)2 * ld)); wq[3] = __builtin_nontemporal_load((const f32x4*)(p + (size_t)3 * ld)); };
;     auto w_cvt = [&]() __attribute__((always_inline)) { unsigned char* t8 = lds + AT_WT + wn4 * WPITCH + 4 * wid;
; #pragma unroll
; DI void attn_unit_d8(unsigned char* lds, const AttnArgs& a) {
;     ...
;     auto tile = [&](const unsigned char* Kb, const unsigned char* Kn, v8i& Pa, v8i& Pb, v8i& v0, v8i& v1, const v8i& Qa, const v8i& Qb, const v8i& w0, const v8i& w1) __attribute__((always_inline)) {
;         qk(Kb, 1, s1a, s1b);
;         v0 = rd32(Kb + voff); v1 = rd32(Kb + voff + 32 * A8_PITCH);
;         o0[0] = mfma8(w0, Qa, o0[0]); o1[0] = mfma8(w0, Qb, o1[0]); o0[1] = mfma8(w1, Qa, o0[1]); o1[1] = mfma8(w1, Qb, o1[1]);
;         expsum(s0a, l0); expsum(s0b, l1); pack4(s0a, Pa, 0); pack4(s0b, Pb, 0);
;         qk(Kn, 0, s0a, s0b);
;         expsum(s1a, l0); expsum(s1b, l1); pack4(s1a, Pa, 4); pack4(s1b, Pb, 4);
; #pragma unroll
;         for (int i = 0; i < 8; ++i) { __builtin_amdgcn_sched_group_barrier(0x008, 1, 0); __builtin_amdgcn_sched_group_barrier(0x402, 22, 0); }
;     };
	v_mfma_f32_32x32x64_f8f6f4 v[66:81], v[192:199], v[114:121], 0
	s_nop 0
	s_nop 0
	s_nop 0
	s_nop 0
	s_nop 0
	s_nop 0
	s_nop 0
	v_cvt_scalef32_pk_fp8_f32 v188, v98, v99, s36
	v_cvt_scalef32_pk_fp8_f32 v189, v102, v103, s36
	v_cvt_scalef32_pk_fp8_f32 v190, v106, v107, s36
	v_cvt_scalef32_pk_fp8_f32 v191, v110, v111, s36
	v_cvt_scalef32_pk_fp8_f32 v158, v82, v83, s36
	v_cvt_scalef32_pk_fp8_f32 v159, v86, v87, s36
	v_pk_add_f32 v[142:143], v[96:97], v[132:133]
	v_pk_add_f32 v[144:145], v[94:95], v[130:131]
	v_cvt_scalef32_pk_fp8_f32 v160, v90, v91, s36
	v_cvt_scalef32_pk_fp8_f32 v188, v100, v101, s36 op_sel:[0,0,0,1]
	v_cvt_scalef32_pk_fp8_f32 v189, v104, v105, s36 op_sel:[0,0,0,1]
	v_cvt_scalef32_pk_fp8_f32 v190, v108, v109, s36 op_sel:[0,0,0,1]
	v_cvt_scalef32_pk_fp8_f32 v191, v112, v113, s36 op_sel:[0,0,0,1]
	v_cvt_scalef32_pk_fp8_f32 v158, v84, v85, s36 op_sel:[0,0,0,1]
	v_cvt_scalef32_pk_fp8_f32 v159, v88, v89, s36 op_sel:[0,0,0,1]
	v_mfma_f32_32x32x64_f8f6f4 v[98:113], v[192:199], v[122:129], 0
	global_load_dwordx2 v[192:193], v[220:221], off
	global_load_dwordx2 v[194:195], v[222:223], off
	ds_read_b128 v[130:133], v219 offset:2560
	ds_read_b128 v[134:137], v219 offset:2576
	s_mulk_i32 s19, 0x2800
	s_nop 0
	v_exp_f32_e32 v146, v66
	s_lshr_b32 s73, s61, 2
	v_exp_f32_e32 v147, v67
	s_lshl_b32 s73, s73, 9
	v_exp_f32_e32 v148, v68
	s_add_i32 s73, s73, s42
	v_exp_f32_e32 v149, v69
	s_mul_i32 s75, s73, 0xaaab
	s_add_i32 s19, s19, 0
	v_cvt_scalef32_pk_fp8_f32 v161, v94, v95, s36
	v_exp_f32_e32 v150, v70
	s_lshr_b32 s75, s75, 22
	v_exp_f32_e32 v151, v71
	s_mul_i32 s76, s75, 0x60
	v_exp_f32_e32 v152, v72
	s_sub_i32 s76, s73, s76
	v_exp_f32_e32 v153, v73
	s_lshr_b32 s77, s76, 6
	v_add_u32_e32 v224, s19, v216
	v_add_u32_e32 v225, s19, v217
	v_cvt_scalef32_pk_fp8_f32 v160, v92, v93, s36 op_sel:[0,0,0,1]
	v_cvt_scalef32_pk_fp8_f32 v161, v96, v97, s36 op_sel:[0,0,0,1]
	v_exp_f32_e32 v196, v74
	s_lshl_b32 s78, s77, 6
	v_exp_f32_e32 v197, v75
	s_sub_i32 s76, s76, s78
	v_exp_f32_e32 v198, v76
	s_sub_i32 s78, 3, s77
	v_exp_f32_e32 v199, v77
	s_lshr_b32 s79, s76, s78
	v_exp_f32_e32 v200, v78
	s_lshl_b32 s79, s79, 2
	v_exp_f32_e32 v201, v79
	s_and_b32 s81, s61, 3
	v_exp_f32_e32 v220, v80
	s_add_i32 s79, s79, s81
	v_exp_f32_e32 v221, v81
	s_lshl_b32 s79, s79, 5
	s_waitcnt lgkmcnt(0)
	v_mfma_f32_32x32x64_f8f6f4 v[82:97], v[130:137], v[114:121], 0
	v_add_f32_e64 v66, v140, v146
	v_add_f32_e64 v67, v141, v147
	v_add_f32_e64 v68, v138, v148
	v_add_f32_e64 v69, v139, v149
	v_add_f32_e64 v66, v150, v66
	v_add_f32_e64 v67, v151, v67
	v_add_f32_e64 v68, v152, v68
	v_add_f32_e64 v69, v153, v69
	v_add_f32_e64 v138, v196, v66
	v_add_f32_e64 v139, v197, v67
	v_add_f32_e64 v140, v198, v68
	v_add_f32_e64 v141, v199, v69
	v_exp_f32_e32 v98, v98
	s_lshl_b32 s81, s63, 2
	v_exp_f32_e32 v99, v99
	s_add_i32 s81, s81, s79
	v_exp_f32_e32 v100, v100
	s_sub_i32 s78, 13, s77
	v_exp_f32_e32 v101, v101
	s_lshl_b32 s81, s81, s78
	v_exp_f32_e32 v102, v102
	s_lshr_b32 s78, 7, s77
	v_exp_f32_e32 v103, v103
	s_and_b32 s78, s76, s78
	v_exp_f32_e32 v104, v104
	s_lshl_b32 s72, s78, 10
	v_exp_f32_e32 v105, v105
	s_add_i32 s81, s81, s72
	v_exp_f32_e32 v106, v106
	s_add_i32 s72, s75, 0
	v_exp_f32_e32 v107, v107
	s_sub_i32 s80, 23, s77
	v_exp_f32_e32 v108, v108
	s_lshl_b32 s72, s72, s80
	v_exp_f32_e32 v109, v109
	s_add_i32 s81, s81, s72
	v_exp_f32_e32 v110, v110
	s_cmp_eq_u32 s77, 0
	s_cselect_b64 s[84:85], s[66:67], s[68:69]
	v_exp_f32_e32 v111, v111
	s_add_u32 s84, s84, s81
	s_addc_u32 s85, s85, 0
	v_exp_f32_e32 v112, v112
	s_lshr_b32 s80, 0x2000, s77
	v_exp_f32_e32 v113, v113
	s_and_b32 s72, s78, 3
	v_mfma_f32_32x32x64_f8f6f4 v[66:81], v[130:137], v[122:129], 0
	v_add_f32_e64 v130, v144, v98
	v_add_f32_e64 v131, v145, v99
	v_add_f32_e64 v132, v142, v100
	v_add_f32_e64 v133, v143, v101
	v_add_f32_e64 v142, v102, v130
	v_add_f32_e64 v143, v103, v131
	v_add_f32_e64 v132, v104, v132
	v_add_f32_e64 v133, v105, v133
	v_add_f32_e64 v134, v220, v140
	v_add_f32_e64 v135, v221, v141
	v_add_f32_e64 v136, v200, v138
	v_add_f32_e64 v137, v201, v139
	s_nop 0
	s_nop 0
	s_nop 0
	s_nop 0
	s_nop 0
	s_nop 0
	v_pk_add_f32 v[142:143], v[106:107], v[142:143]
	v_pk_add_f32 v[132:133], v[108:109], v[132:133]
	v_cvt_scalef32_pk_fp8_f32 v138, v146, v147, s36
	v_cvt_scalef32_pk_fp8_f32 v139, v150, v151, s36
	v_cvt_scalef32_pk_fp8_f32 v140, v196, v197, s36
	v_cvt_scalef32_pk_fp8_f32 v141, v200, v201, s36
	v_cvt_scalef32_pk_fp8_f32 v130, v98, v99, s36
	v_cvt_scalef32_pk_fp8_f32 v131, v102, v103, s36
	v_pk_add_f32 v[146:147], v[112:113], v[132:133]
	v_pk_add_f32 v[150:151], v[110:111], v[142:143]
	v_mfma_f32_32x32x64_f8f6f4 v[50:65], v[170:177], v[184:191], v[50:65]
	v_exp_f32_e32 v82, v82
	s_lshl_b32 s72, s72, 19
	v_exp_f32_e32 v83, v83
	s_lshr_b32 s81, s78, 2
	v_exp_f32_e32 v84, v84
	s_lshl_b32 s81, s81, 17
	v_exp_f32_e32 v85, v85
	s_add_i32 s72, s72, s81
	v_add_u32_e32 v102, s17, v218
; DI unsigned pk4_fp8_mul64(float a, float b, float c, float d) { v2s_t r = {0, 0}; r = __builtin_amdgcn_cvt_scalef32_pk_fp8_f32(r, a, b, 0.015625f, false); r = __builtin_amdgcn_cvt_scalef32_pk_fp8_f32(r, c, d, 0.015625f, true); return __builtin_bit_cast(unsigned, r); }
; DI f32x16 mfma8(v8i a, v8i b, f32x16 c) { return __builtin_amdgcn_mfma_scale_f32_32x32x64_f8f6f4(a, b, c, 0, 0, 0, 0, 0, 0); }
; DI void attn_unit_a8(unsigned char* lds, const AttnArgs& a) {
;     ...
;     auto w_cvt = [&]() __attribute__((always_inline)) { unsigned char* t8 = lds + AT_WT + wn4 * WPITCH + 4 * wid;
; #pragma unroll
;         for (int j = 0; j < 4; ++j) *(unsigned*)(t8 + j * WPITCH) = pk4_fp8_mul64(wq[0][j], wq[1][j], wq[2][j], wq[3][j]); };
;     const int wcol = tid >> 1, whalf = tid & 1;
;     const unsigned wper_gu = (unsigned)((wcol >> 7) * 256 + (wcol & 96) + invperm32(wcol & 31)) * 1024u + 16u * whalf;
;     const unsigned wper_dn = (unsigned)fwd_lane16(wcol) * 1024u + 16u * whalf;
;     auto w_store = [&](int j) __attribute__((always_inline)) { const float* src; unsigned char* dst; int ld, n0, k0; bool gu; w_decode(j, src, dst, ld, n0, k0, gu);
;         const int nb = n0 >> 8; const unsigned uni = (unsigned)(gu ? (nb & 3) * 512 + (nb >> 2) * 128 : nb * 256) * 1024u + (unsigned)k0;
;         const unsigned off = (gu ? wper_gu : wper_dn) + uni;
;         const unsigned* t = (const unsigned*)(lds + AT_WT + wcol * WPITCH + 16 * whalf);
;         *(u32x4*)(dst + off) = (u32x4){t[0], t[1], t[2], t[3]}; };
; DI void attn_unit_d8(unsigned char* lds, const AttnArgs& a) {
;     ...
;     auto tile = [&](const unsigned char* Kb, const unsigned char* Kn, v8i& Pa, v8i& Pb, v8i& v0, v8i& v1, const v8i& Qa, const v8i& Qb, const v8i& w0, const v8i& w1) __attribute__((always_inline)) {
;         qk(Kb, 1, s1a, s1b);
;         v0 = rd32(Kb + voff); v1 = rd32(Kb + voff + 32 * A8_PITCH);
;         o0[0] = mfma8(w0, Qa, o0[0]); o1[0] = mfma8(w0, Qb, o1[0]); o0[1] = mfma8(w1, Qa, o0[1]); o1[1] = mfma8(w1, Qb, o1[1]);
;         expsum(s0a, l0); expsum(s0b, l1); pack4(s0a, Pa, 0); pack4(s0b, Pb, 0);
;         qk(Kn, 0, s0a, s0b);
;         expsum(s1a, l0); expsum(s1b, l1); pack4(s1a, Pa, 4); pack4(s1b, Pb, 4);
; #pragma unroll
;         for (int i = 0; i < 8; ++i) { __builtin_amdgcn_sched_group_barrier(0x008, 1, 0); __builtin_amdgcn_sched_group_barrier(0x402, 22, 0); }
;     };
	v_exp_f32_e32 v86, v86
	s_lshl_b32 s81, s78, 18
	v_exp_f32_e32 v87, v87
	s_cmp_eq_u32 s77, 0
	s_cselect_b32 s72, s72, s81
	v_exp_f32_e32 v88, v88
	s_mul_i32 s81, s77, 0x10000000
	v_exp_f32_e32 v89, v89
	s_add_i32 s81, s81, 0x1094000
	v_cvt_scalef32_pk_fp8_f32 v130, v100, v101, s36 op_sel:[0,0,0,1]
	v_cvt_scalef32_pk_fp8_f32 v131, v104, v105, s36 op_sel:[0,0,0,1]
	v_exp_f32_e32 v90, v90
	s_add_i32 s72, s72, s79
	v_exp_f32_e32 v91, v91
	s_sub_i32 s73, 21, s77
	v_exp_f32_e32 v92, v92
	s_lshl_b32 s73, s75, s73
	v_exp_f32_e32 v93, v93
	s_add_i32 s72, s72, s73
	ds_read_b128 v[98:101], v102
	ds_read_b128 v[102:105], v102 offset:16
	s_nop 0
	v_cvt_scalef32_pk_fp8_f32 v138, v148, v149, s36 op_sel:[0,0,0,1]
	v_cvt_scalef32_pk_fp8_f32 v139, v152, v153, s36 op_sel:[0,0,0,1]
	v_cvt_scalef32_pk_fp8_f32 v140, v198, v199, s36 op_sel:[0,0,0,1]
	v_cvt_scalef32_pk_fp8_f32 v141, v220, v221, s36 op_sel:[0,0,0,1]
	s_nop 0
	v_exp_f32_e32 v94, v94
	s_add_u32 s72, s72, s81
	v_mfma_f32_32x32x64_f8f6f4 v[2:17], v[170:177], v[154:161], v[2:17]
	v_exp_f32_e32 v148, v96
	s_or_b32 s79, s72, s77
	v_cvt_scalef32_pk_fp8_f32 v132, v106, v107, s36
	v_exp_f32_e32 v149, v97
	v_pk_add_f32 v[96:97], v[136:137], v[82:83]
	v_pk_add_f32 v[106:107], v[134:135], v[84:85]
	v_exp_f32_e32 v66, v66
	v_exp_f32_e32 v67, v67
	v_exp_f32_e32 v68, v68
	v_exp_f32_e32 v69, v69
	v_exp_f32_e32 v95, v95
	v_cvt_scalef32_pk_fp8_f32 v133, v110, v111, s36
	v_pk_add_f32 v[106:107], v[88:89], v[106:107]
	v_pk_add_f32 v[96:97], v[86:87], v[96:97]
	v_exp_f32_e32 v70, v70
	v_exp_f32_e32 v71, v71
	v_exp_f32_e32 v72, v72
	v_exp_f32_e32 v73, v73
	v_cvt_scalef32_pk_fp8_f32 v132, v108, v109, s36 op_sel:[0,0,0,1]
	v_cvt_scalef32_pk_fp8_f32 v133, v112, v113, s36 op_sel:[0,0,0,1]
	v_pk_add_f32 v[96:97], v[90:91], v[96:97]
	v_pk_add_f32 v[106:107], v[92:93], v[106:107]
	v_exp_f32_e32 v74, v74
	v_mfma_f32_32x32x64_f8f6f4 v[34:49], v[162:169], v[184:191], v[34:49]
	v_exp_f32_e32 v75, v75
	v_exp_f32_e32 v76, v76
	v_exp_f32_e32 v77, v77
	v_exp_f32_e32 v78, v78
	v_exp_f32_e32 v79, v79
	s_nop 0
	v_exp_f32_e32 v80, v80
	v_exp_f32_e32 v81, v81
	s_nop 0
	s_nop 0
	v_cvt_scalef32_pk_fp8_f32 v142, v82, v83, s36
	s_nop 0
	v_cvt_scalef32_pk_fp8_f32 v143, v86, v87, s36
	v_cvt_scalef32_pk_fp8_f32 v144, v90, v91, s36
	v_cvt_scalef32_pk_fp8_f32 v142, v84, v85, s36 op_sel:[0,0,0,1]
	v_pk_add_f32 v[82:83], v[150:151], v[66:67]
	v_pk_add_f32 v[84:85], v[146:147], v[68:69]
	s_mulk_i32 s49, 0x2800
	v_pk_add_f32 v[184:185], v[148:149], v[106:107]
	v_pk_add_f32 v[186:187], v[94:95], v[96:97]
	v_cvt_scalef32_pk_fp8_f32 v145, v94, v95, s36
	v_cvt_scalef32_pk_fp8_f32 v143, v88, v89, s36 op_sel:[0,0,0,1]
	v_cvt_scalef32_pk_fp8_f32 v144, v92, v93, s36 op_sel:[0,0,0,1]
	v_mfma_f32_32x32x64_f8f6f4 v[18:33], v[162:169], v[154:161], v[18:33]
	v_add_f32_e64 v84, v72, v84
	v_add_f32_e64 v85, v73, v85
	v_add_f32_e64 v82, v70, v82
	v_add_f32_e64 v83, v71, v83
	s_nop 0
	s_nop 0
	s_nop 0
	s_nop 0
	s_add_i32 s6, s49, 0
	v_add_f32_e64 v82, v74, v82
	v_add_f32_e64 v83, v75, v83
	v_add_f32_e64 v84, v76, v84
	v_add_f32_e64 v85, v77, v85
	v_cvt_scalef32_pk_fp8_f32 v134, v66, v67, s36
	v_cvt_scalef32_pk_fp8_f32 v135, v70, v71, s36
	v_cvt_scalef32_pk_fp8_f32 v136, v74, v75, s36
	v_cvt_scalef32_pk_fp8_f32 v137, v78, v79, s36
	v_pk_add_f32 v[188:189], v[80:81], v[84:85]
	v_pk_add_f32 v[190:191], v[78:79], v[82:83]
	v_add_u32_e32 v106, s6, v216
	v_add_u32_e32 v107, s6, v217
	v_cvt_scalef32_pk_fp8_f32 v145, v148, v149, s36 op_sel:[0,0,0,1]
	v_cvt_scalef32_pk_fp8_f32 v134, v68, v69, s36 op_sel:[0,0,0,1]
	v_cvt_scalef32_pk_fp8_f32 v135, v72, v73, s36 op_sel:[0,0,0,1]
	v_cvt_scalef32_pk_fp8_f32 v136, v76, v77, s36 op_sel:[0,0,0,1]
	v_cvt_scalef32_pk_fp8_f32 v137, v80, v81, s36 op_sel:[0,0,0,1]
	s_waitcnt lgkmcnt(0)
	v_mfma_f32_32x32x64_f8f6f4 v[82:97], v[98:105], v[114:121], 0
	ds_read_b128 v[154:157], v219 offset:5120
	ds_read_b128 v[158:161], v219 offset:5136
	ds_read_b128 v[146:149], v219 offset:7680
	ds_read_b128 v[150:153], v219 offset:7696
	s_cmpk_gt_i32 s42, 0x1ff
	s_cbranch_scc1 .Lmy_rd0_ldum
	s_add_i32 s72, s61, -1
	s_cmp_lt_u32 s72, 24
	s_cbranch_scc0 .Lmy_rd0_noc
	s_waitcnt vmcnt(4)
	v_cvt_scalef32_pk_fp8_f32 v236, v236, v240, s62
	v_cvt_scalef32_pk_fp8_f32 v237, v237, v241, s62
	v_cvt_scalef32_pk_fp8_f32 v238, v238, v242, s62
	v_cvt_scalef32_pk_fp8_f32 v239, v239, v243, s62
	v_cvt_scalef32_pk_fp8_f32 v236, v244, v248, s62 op_sel:[0,0,0,1]
	v_cvt_scalef32_pk_fp8_f32 v237, v245, v249, s62 op_sel:[0,0,0,1]
	v_cvt_scalef32_pk_fp8_f32 v238, v246, v250, s62 op_sel:[0,0,0,1]
	v_cvt_scalef32_pk_fp8_f32 v239, v247, v251, s62 op_sel:[0,0,0,1]
	ds_write_b32 v252, v236
	ds_write_b32 v252, v237 offset:36
	ds_write_b32 v252, v238 offset:72
	ds_write_b32 v252, v239 offset:108
.Lmy_rd0_noc:
	ds_read2_b32 v[244:245], v253 offset1:1
	ds_read2_b32 v[246:247], v253 offset0:2 offset1:3
	s_cmp_lt_u32 s61, 24
	s_cbranch_scc1 .Lmy_rd0_lgo

; DI unsigned pk4_fp8_mul64(float a, float b, float c, float d) { v2s_t r = {0, 0}; r = __builtin_amdgcn_cvt_scalef32_pk_fp8_f32(r, a, b, 0.015625f, false); r = __builtin_amdgcn_cvt_scalef32_pk_fp8_f32(r, c, d, 0.015625f, true); return __builtin_bit_cast(unsigned, r); }
; DI void attn_unit_a8(unsigned char* lds, const AttnArgs& a) {
;     ...
;     auto w_issue = [&](int j) __attribute__((always_inline)) { const float* src; unsigned char* dst; int ld, n0, k0; bool gu; w_decode(j, src, dst, ld, n0, k0, gu);
;         const float* p = src + (size_t)(k0 + 4 * wid) * ld + n0 + wn4;
;         wq[0] = __builtin_nontemporal_load((const f32x4*)p); wq[1] = __builtin_nontemporal_load((const f32x4*)(p + ld));
;         wq[2] = __builtin_nontemporal_load((const f32x4*)(p + (size_t)2 * ld)); wq[3] = __builtin_nontemporal_load((const f32x4*)(p + (size_t)3 * ld)); };
;     auto w_cvt = [&]() __attribute__((always_inline)) { unsigned char* t8 = lds + AT_WT + wn4 * WPITCH + 4 * wid;
; #pragma unroll
;         for (int j = 0; j < 4; ++j) *(unsigned*)(t8 + j * WPITCH) = pk4_fp8_mul64(wq[0][j], wq[1][j], wq[2][j], wq[3][j]); };
;     const int wcol = tid >> 1, whalf = tid & 1;
;     const unsigned wper_gu = (unsigned)((wcol >> 7) * 256 + (wcol & 96) + invperm32(wcol & 31)) * 1024u + 16u * whalf;
;     const unsigned wper_dn = (unsigned)fwd_lane16(wcol) * 1024u + 16u * whalf;
;     auto w_store = [&](int j) __attribute__((always_inline)) { const float* src; unsigned char* dst; int ld, n0, k0; bool gu; w_decode(j, src, dst, ld, n0, k0, gu);
;         const int nb = n0 >> 8; const unsigned uni = (unsigned)(gu ? (nb & 3) * 512 + (nb >> 2) * 128 : nb * 256) * 1024u + (unsigned)k0;
;         const unsigned off = (gu ? wper_gu : wper_dn) + uni;
;         const unsigned* t = (const unsigned*)(lds + AT_WT + wcol * WPITCH + 16 * whalf);
;         *(u32x4*)(dst + off) = (u32x4){t[0], t[1], t[2], t[3]}; };
.Lmy_rd0_lgo:
	global_load_dwordx4 v[236:239], v235, s[84:85] nt
	s_add_u32 s84, s84, s80
	s_addc_u32 s85, s85, 0
	global_load_dwordx4 v[240:243], v235, s[84:85] nt
	s_add_u32 s84, s84, s80
	s_addc_u32 s85, s85, 0
	s_cmpk_gt_i32 s42, 0x1ff
	s_cbranch_scc1 .Lmy_rd0_sdum
	s_add_i32 s72, s61, -2
	s_cmp_lt_u32 s72, 24
	s_cbranch_scc0 .Lmy_rd0_sdum
	s_andn2_b32 s73, s65, 1
	s_add_u32 s82, s70, s73
	s_addc_u32 s83, s71, 0
	s_bitcmp1_b32 s65, 0
	s_cbranch_scc1 .Lmy_rd0_sdn
	s_waitcnt lgkmcnt(0)
	global_store_dwordx4 v254, v[244:247], s[82:83]
	s_branch .Lmy_rd0_sdone
.Lmy_rd0_sdn:
	s_waitcnt lgkmcnt(0)
	global_store_dwordx4 v255, v[244:247], s[82:83]
	s_branch .Lmy_rd0_sdone

; DI f32x16 mfma8(v8i a, v8i b, f32x16 c) { return __builtin_amdgcn_mfma_scale_f32_32x32x64_f8f6f4(a, b, c, 0, 0, 0, 0, 0, 0); }
; DI void attn_unit_a8(unsigned char* lds, const AttnArgs& a) {
;     ...
;     auto w_issue = [&](int j) __attribute__((always_inline)) { const float* src; unsigned char* dst; int ld, n0, k0; bool gu; w_decode(j, src, dst, ld, n0, k0, gu);
;         const float* p = src + (size_t)(k0 + 4 * wid) * ld + n0 + wn4;
;         wq[0] = __builtin_nontemporal_load((const f32x4*)p); wq[1] = __builtin_nontemporal_load((const f32x4*)(p + ld));
;         wq[2] = __builtin_nontemporal_load((const f32x4*)(p + (size_t)2 * ld)); wq[3] = __builtin_nontemporal_load((const f32x4*)(p + (size_t)3 * ld)); };
; DI void attn_unit_d8(unsigned char* lds, const AttnArgs& a) {
;     ...
;         lstore(s3, kreg0, vreg0); lstore(s4, kreg1, vreg1);
;         __syncthreads();
;         sb = s2;
;     }
;     o0[0] = mfma8(vY0, PaY, o0[0]); o1[0] = mfma8(vY0, PbY, o1[0]); o0[1] = mfma8(vY1, PaY, o0[1]); o1[1] = mfma8(vY1, PbY, o1[1]);
;     __builtin_amdgcn_s_setprio(0);
;     float lt0 = l0[0] + l0[1] + l0[2] + l0[3]; lt0 += __shfl_xor(lt0, 32);
;     float lt1 = l1[0] + l1[1] + l1[2] + l1[3]; lt1 += __shfl_xor(lt1, 32);
;     unsigned char* op = a.out8 + (size_t)(wid * 32 + r) * 1024 + 4 * h;
;     const float r0 = 16.0f / lt0, r1 = 16.0f * a.lam / lt1;
;     float ss = 0.f;
; #pragma unroll
;     for (int d = 0; d < 2; ++d)
; #pragma unroll
;         for (int i = 0; i < 16; ++i) { const float v = o0[d][i] * r0 - o1[d][i] * r1; o0[d][i] = v; ss += v * v; }
;     ss += __shfl_xor(ss, 32);
;     const float rinv = rsqrtf(ss * (1.0f / 64.0f) + EPS) * a.oscale * CAT_SCALE;
.Lmy_rd0_sdone:
	s_nop 0
	global_load_dwordx4 v[244:247], v235, s[84:85] nt
	s_add_u32 s84, s84, s80
	s_addc_u32 s85, s85, 0
	global_load_dwordx4 v[248:251], v235, s[84:85] nt
	s_mov_b32 s65, s58
	s_mov_b32 s58, s79
	v_xor_b32_e32 v252, 0x4000, v252
	v_xor_b32_e32 v253, 0x4000, v253
	s_add_i32 s61, s61, 1
	s_add_i32 s18, s46, 2
	s_cmpk_lt_u32 s46, 0x42
	s_mov_b32 s46, s18
	s_waitcnt vmcnt(6)
	ds_write_b64 v224, v[192:193]
	v_mfma_f32_32x32x64_f8f6f4 v[66:81], v[98:105], v[122:129], 0
	v_add_u32_e32 v98, 0x1400, v225
	v_add_u32_e32 v99, 0x1400, v107
	ds_write2_b32 v98, v202, v203 offset1:8
	s_waitcnt vmcnt(5)
	ds_write_b64 v106, v[194:195]
	ds_write2_b32 v99, v204, v205 offset1:8
	s_waitcnt lgkmcnt(0)
	s_barrier
	s_cbranch_scc1 .LBB0_663
	s_lshl_b64 s[14:15], s[14:15], 10
	s_add_u32 s6, s8, s14
	s_addc_u32 s15, s9, s15
	s_add_u32 s14, s6, s43
	v_mfma_f32_32x32x64_f8f6f4 v[50:65], v[154:161], v[138:145], v[50:65]
	s_addc_u32 s15, s15, 0
	v_mfma_f32_32x32x64_f8f6f4 v[2:17], v[154:161], v[130:137], v[2:17]
	v_mfma_f32_32x32x64_f8f6f4 v[34:49], v[146:153], v[138:145], v[34:49]
	v_mfma_f32_32x32x64_f8f6f4 v[18:33], v[146:153], v[130:137], v[18:33]
	s_setprio 0
	v_add_f32_e32 v66, v186, v187
	v_add_f32_e32 v66, v184, v66
	v_add_f32_e32 v66, v185, v66
	ds_bpermute_b32 v67, v1, v66
	v_add_f32_e32 v68, v190, v191
	v_add_f32_e32 v68, v188, v68
	v_add_f32_e32 v68, v189, v68
	ds_bpermute_b32 v69, v1, v68
	s_waitcnt lgkmcnt(1)
	v_add_f32_e32 v66, v66, v67
	v_div_scale_f32 v67, s[16:17], v66, v66, s36
	v_rcp_f32_e32 v70, v67
	s_waitcnt lgkmcnt(0)
	v_add_f32_e32 v68, v68, v69
	v_lshlrev_b32_e32 v178, 2, v214
	s_add_i32 s42, s42, s64
	v_fma_f32 v69, -v67, v70, 1.0
	v_fmac_f32_e32 v70, v69, v70
	v_div_scale_f32 v69, vcc, s36, v66, s36
	v_mul_f32_e32 v71, v69, v70
	v_fma_f32 v72, -v67, v71, v69
	v_fmac_f32_e32 v71, v72, v70
	v_fma_f32 v67, -v67, v71, v69
	v_div_scale_f32 v69, s[16:17], v68, v68, v211
	v_rcp_f32_e32 v72, v69
	v_div_fmas_f32 v67, v67, v70, v71
	v_div_fixup_f32 v66, v67, v66, s36
	s_cmpk_gt_i32 s42, 0x21f
	v_fma_f32 v67, -v69, v72, 1.0
	v_fmac_f32_e32 v72, v67, v72
	v_div_scale_f32 v67, vcc, v211, v68, v211
	v_mul_f32_e32 v70, v67, v72
	v_fma_f32 v71, -v69, v70, v67
	v_fmac_f32_e32 v70, v71, v72
	v_fma_f32 v67, -v69, v70, v67
	v_div_fmas_f32 v67, v67, v72, v70
	v_div_fixup_f32 v68, v67, v68, v211
	v_mul_f32_e32 v2, v2, v68
	v_fma_f32 v50, v50, v66, -v2
	v_mul_f32_e32 v2, v3, v68
	v_fma_f32 v51, v51, v66, -v2
	v_mul_f32_e32 v67, v51, v51
	v_mul_f32_e32 v2, v4, v68
	v_fmac_f32_e32 v67, v50, v50
	v_fma_f32 v52, v52, v66, -v2
	v_mul_f32_e32 v2, v5, v68
	v_fmac_f32_e32 v67, v52, v52
	v_fma_f32 v53, v53, v66, -v2
	v_mul_f32_e32 v2, v6, v68
	v_fmac_f32_e32 v67, v53, v53
	v_fma_f32 v54, v54, v66, -v2
	v_mul_f32_e32 v2, v7, v68
	v_fmac_f32_e32 v67, v54, v54
	v_fma_f32 v55, v55, v66, -v2
	v_mul_f32_e32 v2, v8, v68
	v_fmac_f32_e32 v67, v55, v55
	v_fma_f32 v56, v56, v66, -v2
	v_mul_f32_e32 v2, v9, v68
	v_fmac_f32_e32 v67, v56, v56
	v_fma_f32 v57, v57, v66, -v2
	v_mul_f32_e32 v2, v10, v68
	v_fmac_f32_e32 v67, v57, v57
	v_fma_f32 v58, v58, v66, -v2
	v_mul_f32_e32 v2, v11, v68
	v_fmac_f32_e32 v67, v58, v58
	v_fma_f32 v59, v59, v66, -v2
	v_mul_f32_e32 v2, v12, v68
	v_fmac_f32_e32 v67, v59, v59
	v_fma_f32 v60, v60, v66, -v2
	v_mul_f32_e32 v2, v13, v68
	v_fmac_f32_e32 v67, v60, v60
	v_fma_f32 v61, v61, v66, -v2
	v_mul_f32_e32 v14, v14, v68
	v_fmac_f32_e32 v67, v61, v61
	v_fma_f32 v62, v62, v66, -v14
	v_mul_f32_e32 v14, v15, v68
	v_fmac_f32_e32 v67, v62, v62
	v_fma_f32 v63, v63, v66, -v14
	v_mul_f32_e32 v14, v16, v68
	v_lshlrev_b32_e32 v69, 4, v214
	v_fmac_f32_e32 v67, v63, v63
	v_fma_f32 v64, v64, v66, -v14
	v_mul_f32_e32 v14, v17, v68
	global_load_dwordx4 v[2:5], v69, s[10:11] offset:224
	global_load_dwordx4 v[6:9], v69, s[10:11] offset:32
	global_load_dwordx4 v[10:13], v69, s[10:11]
	v_fmac_f32_e32 v67, v64, v64
	v_fma_f32 v65, v65, v66, -v14
	v_mul_f32_e32 v14, v18, v68
	v_fmac_f32_e32 v67, v65, v65
	v_fma_f32 v70, v34, v66, -v14
	v_mul_f32_e32 v14, v19, v68
	v_fmac_f32_e32 v67, v70, v70
	v_fma_f32 v71, v35, v66, -v14
	v_mul_f32_e32 v14, v20, v68
	v_fmac_f32_e32 v67, v71, v71
	v_fma_f32 v72, v36, v66, -v14
	v_mul_f32_e32 v14, v21, v68
	v_fmac_f32_e32 v67, v72, v72
	v_fma_f32 v73, v37, v66, -v14
	v_mul_f32_e32 v14, v22, v68
	v_fmac_f32_e32 v67, v73, v73
	v_fma_f32 v74, v38, v66, -v14
	v_mul_f32_e32 v14, v23, v68
	v_fmac_f32_e32 v67, v74, v74
	v_fma_f32 v75, v39, v66, -v14
	v_fmac_f32_e32 v67, v75, v75
	v_pk_mul_f32 v[14:15], v[24:25], v[68:69] op_sel_hi:[1,0]
	v_pk_mul_f32 v[22:23], v[32:33], v[68:69] op_sel_hi:[1,0]
	v_pk_fma_f32 v[34:35], v[40:41], v[66:67], v[14:15] op_sel_hi:[1,0,1] neg_lo:[0,0,1] neg_hi:[0,0,1]
	s_nop 0
	v_pk_mul_f32 v[14:15], v[34:35], v[34:35]
	s_nop 0
	v_add_f32_e32 v14, v14, v67
	v_add_f32_e32 v20, v15, v14
	v_pk_mul_f32 v[14:15], v[26:27], v[68:69] op_sel_hi:[1,0]
	s_nop 0
	v_pk_fma_f32 v[36:37], v[42:43], v[66:67], v[14:15] op_sel_hi:[1,0,1] neg_lo:[0,0,1] neg_hi:[0,0,1]
	global_load_dwordx4 v[14:17], v69, s[10:11] offset:64
	v_pk_mul_f32 v[18:19], v[36:37], v[36:37]
	v_pk_fma_f32 v[42:43], v[48:49], v[66:67], v[22:23] op_sel_hi:[1,0,1] neg_lo:[0,0,1] neg_hi:[0,0,1]
	v_add_f32_e32 v18, v18, v20
	v_add_f32_e32 v20, v19, v18
	v_pk_mul_f32 v[18:19], v[28:29], v[68:69] op_sel_hi:[1,0]
	v_pk_mul_f32 v[22:23], v[42:43], v[42:43]
	v_pk_fma_f32 v[38:39], v[44:45], v[66:67], v[18:19] op_sel_hi:[1,0,1] neg_lo:[0,0,1] neg_hi:[0,0,1]
	s_nop 0
	v_pk_mul_f32 v[18:19], v[38:39], v[38:39]
	s_nop 0
	v_add_f32_e32 v18, v18, v20
	v_add_f32_e32 v20, v19, v18
	v_pk_mul_f32 v[18:19], v[30:31], v[68:69] op_sel_hi:[1,0]
	s_nop 0
	v_pk_fma_f32 v[40:41], v[46:47], v[66:67], v[18:19] op_sel_hi:[1,0,1] neg_lo:[0,0,1] neg_hi:[0,0,1]
	s_nop 0
	v_pk_mul_f32 v[18:19], v[40:41], v[40:41]
	s_nop 0
	v_add_f32_e32 v18, v18, v20
	v_add_f32_e32 v24, v19, v18
	v_add_f32_e32 v22, v22, v24
	v_add_f32_e32 v26, v23, v22
	ds_bpermute_b32 v27, v1, v26
	global_load_dwordx4 v[18:21], v69, s[10:11] offset:96
	global_load_dwordx4 v[22:25], v69, s[10:11] offset:192
	s_waitcnt lgkmcnt(0)
; DI unsigned pk4_fp8(float a, float b, float c, float d) { int r = 0; r = __builtin_amdgcn_cvt_pk_fp8_f32(a, b, r, false); r = __builtin_amdgcn_cvt_pk_fp8_f32(c, d, r, true); return (unsigned)r; }
; DI float clamp448(float x) { return __builtin_amdgcn_fmed3f(x, -448.0f, 448.0f); }
; DI void attn_unit_d8(unsigned char* lds, const AttnArgs& a) {
;     ...
;     const float r0 = 16.0f / lt0, r1 = 16.0f * a.lam / lt1;
;     float ss = 0.f;
; #pragma unroll
;     for (int d = 0; d < 2; ++d)
; #pragma unroll
;         for (int i = 0; i < 16; ++i) { const float v = o0[d][i] * r0 - o1[d][i] * r1; o0[d][i] = v; ss += v * v; }
;     ss += __shfl_xor(ss, 32);
;     const float rinv = rsqrtf(ss * (1.0f / 64.0f) + EPS) * a.oscale * CAT_SCALE;
;     f32x4 ggv[2][4];
; #pragma unroll
;     for (int d = 0; d < 2; ++d)
; #pragma unroll
;         for (int g = 0; g < 4; ++g) ggv[d][g] = *(const f32x4*)(a.subg + 32 * d + 8 * g + 4 * h);
;     asm volatile("" : "+v"(ggv[0][0]), "+v"(ggv[1][3]));
; #pragma unroll
;     for (int d = 0; d < 2; ++d)
; #pragma unroll
;         for (int g = 0; g < 4; ++g) { const f32x4 gg = ggv[d][g];
;             *(unsigned*)(op + 32 * d + 8 * g) = pk4_fp8(clamp448(o0[d][4 * g] * rinv * gg[0]), clamp448(o0[d][4 * g + 1] * rinv * gg[1]), clamp448(o0[d][4 * g + 2] * rinv * gg[2]), clamp448(o0[d][4 * g + 3] * rinv * gg[3])); }
	v_add_f32_e32 v26, v26, v27
	v_fmamk_f32 v26, v26, 0x3c800000, v212
	v_mul_f32_e32 v27, 0x4b800000, v26
	v_cmp_gt_f32_e32 vcc, s39, v26
	s_nop 1
	v_cndmask_b32_e32 v30, v26, v27, vcc
	global_load_dwordx4 v[26:29], v69, s[10:11] offset:128
	v_rsq_f32_e32 v32, v30
	v_lshlrev_b64 v[30:31], 10, v[180:181]
	v_lshl_add_u64 v[44:45], s[14:15], 0, v[30:31]
	v_lshl_add_u64 v[44:45], v[44:45], 0, v[178:179]
	v_mul_f32_e32 v30, 0x45800000, v32
	v_cndmask_b32_e32 v30, v32, v30, vcc
	v_mul_f32_e32 v48, 0x3f4ccccd, v30
	global_load_dwordx4 v[30:33], v69, s[10:11] offset:160
	v_mul_f32_e32 v48, 0x41800000, v48
	s_waitcnt vmcnt(5)
	v_mul_f32_e32 v49, v50, v48
	v_mul_f32_e32 v10, v10, v49
	v_mul_f32_e32 v49, v51, v48
	v_mul_f32_e32 v11, v11, v49
	v_mul_f32_e32 v49, v52, v48
	v_med3_f32 v10, v10, s40, v213
	v_med3_f32 v11, v11, s40, v213
	v_mul_f32_e32 v12, v12, v49
	s_nop 0
	v_cvt_pk_fp8_f32 v49, v10, v11
	v_mul_f32_e32 v10, v53, v48
	v_mul_f32_e32 v10, v13, v10
	v_med3_f32 v12, v12, s40, v213
	v_med3_f32 v10, v10, s40, v213
	v_cvt_pk_fp8_f32 v49, v12, v10 op_sel:[0,0,1]
	v_mul_f32_e32 v10, v54, v48
	v_mul_f32_e32 v6, v6, v10
	v_mul_f32_e32 v10, v55, v48
	v_mul_f32_e32 v7, v7, v10
	v_mul_f32_e32 v10, v56, v48
	v_med3_f32 v6, v6, s40, v213
	v_med3_f32 v7, v7, s40, v213
	v_mul_f32_e32 v8, v8, v10
	s_nop 0
	v_cvt_pk_fp8_f32 v10, v6, v7
	v_mul_f32_e32 v6, v57, v48
	v_mul_f32_e32 v6, v9, v6
	v_med3_f32 v8, v8, s40, v213
	v_med3_f32 v6, v6, s40, v213
	v_cvt_pk_fp8_f32 v10, v8, v6 op_sel:[0,0,1]
	v_add_co_u32_e32 v6, vcc, s41, v44
	v_lshl_add_u64 v[46:47], v[44:45], 0, s[12:13]
	s_nop 0
	v_addc_co_u32_e32 v7, vcc, 0, v45, vcc
	global_store_dword v[6:7], v49, off offset:768
	global_store_dword v[46:47], v10, off offset:8
	v_mul_f32_e32 v6, v58, v48
	v_mul_f32_e32 v7, v59, v48
	s_waitcnt vmcnt(6)
	v_mul_f32_e32 v6, v14, v6
	v_mul_f32_e32 v7, v15, v7
	v_med3_f32 v6, v6, s40, v213
	v_med3_f32 v7, v7, s40, v213
	s_nop 0
	v_cvt_pk_fp8_f32 v9, v6, v7
	v_mul_f32_e32 v8, v60, v48
	v_mul_f32_e32 v6, v61, v48
	v_mul_f32_e32 v8, v16, v8
	v_mul_f32_e32 v6, v17, v6
	v_med3_f32 v8, v8, s40, v213
	v_med3_f32 v6, v6, s40, v213
	v_cvt_pk_fp8_f32 v9, v8, v6 op_sel:[0,0,1]
	v_mul_f32_e32 v6, v62, v48
	v_mul_f32_e32 v7, v63, v48
	s_nop 0
	v_mul_f32_e32 v8, v64, v48
	s_nop 0
	s_waitcnt vmcnt(5)
	v_mul_f32_e32 v6, v18, v6
	v_mul_f32_e32 v7, v19, v7
	v_med3_f32 v6, v6, s40, v213
	v_med3_f32 v7, v7, s40, v213
	v_cvt_pk_fp8_f32 v10, v6, v7
	v_mul_f32_e32 v6, v65, v48
	v_mul_f32_e32 v8, v20, v8
	v_mul_f32_e32 v6, v21, v6
	v_med3_f32 v8, v8, s40, v213
	v_med3_f32 v6, v6, s40, v213
	v_cvt_pk_fp8_f32 v10, v8, v6 op_sel:[0,0,1]
	v_mul_f32_e32 v6, v70, v48
	v_mul_f32_e32 v7, v71, v48
	s_waitcnt vmcnt(3)
	v_mul_f32_e32 v6, v26, v6
	v_mul_f32_e32 v7, v27, v7
	v_med3_f32 v6, v6, s40, v213
	v_med3_f32 v7, v7, s40, v213
	v_cvt_pk_fp8_f32 v11, v6, v7
	v_mul_f32_e32 v8, v72, v48
	v_mul_f32_e32 v6, v73, v48
	v_mul_f32_e32 v8, v28, v8
	v_mul_f32_e32 v6, v29, v6
	v_med3_f32 v8, v8, s40, v213
	v_med3_f32 v6, v6, s40, v213
	v_cvt_pk_fp8_f32 v11, v8, v6 op_sel:[0,0,1]
	v_mul_f32_e32 v6, v74, v48
	v_mul_f32_e32 v7, v75, v48
	s_waitcnt vmcnt(2)
	v_mul_f32_e32 v6, v30, v6
	v_mul_f32_e32 v7, v31, v7
	v_med3_f32 v6, v6, s40, v213
	v_med3_f32 v7, v7, s40, v213
	s_nop 0
	v_cvt_pk_fp8_f32 v12, v6, v7
	v_mul_f32_e32 v8, v34, v48
	v_mul_f32_e32 v6, v35, v48
	v_mul_f32_e32 v8, v32, v8
	v_mul_f32_e32 v6, v33, v6
	v_med3_f32 v8, v8, s40, v213
	v_med3_f32 v6, v6, s40, v213
	v_cvt_pk_fp8_f32 v12, v8, v6 op_sel:[0,0,1]
	v_mul_f32_e32 v6, v36, v48
	v_mul_f32_e32 v7, v37, v48
	v_mul_f32_e32 v6, v22, v6
	v_mul_f32_e32 v7, v23, v7
	global_store_dword v[46:47], v9, off offset:16
	global_store_dword v[46:47], v10, off offset:24
	global_store_dword v[46:47], v11, off offset:32
	global_store_dword v[46:47], v12, off offset:40
	v_med3_f32 v6, v6, s40, v213
	v_med3_f32 v7, v7, s40, v213
	s_nop 0
	v_cvt_pk_fp8_f32 v9, v6, v7
	v_mul_f32_e32 v8, v38, v48
	v_mul_f32_e32 v6, v39, v48
	v_mul_f32_e32 v8, v24, v8
	v_mul_f32_e32 v6, v25, v6
	v_med3_f32 v8, v8, s40, v213
	v_med3_f32 v6, v6, s40, v213
	v_cvt_pk_fp8_f32 v9, v8, v6 op_sel:[0,0,1]
	v_mul_f32_e32 v6, v40, v48
	v_mul_f32_e32 v2, v2, v6
	v_mul_f32_e32 v6, v41, v48
	v_mul_f32_e32 v3, v3, v6
	v_mul_f32_e32 v6, v42, v48
	v_med3_f32 v2, v2, s40, v213
	v_med3_f32 v3, v3, s40, v213
	v_mul_f32_e32 v4, v4, v6
	s_nop 0
	v_cvt_pk_fp8_f32 v6, v2, v3
	v_mul_f32_e32 v2, v43, v48
	v_mul_f32_e32 v2, v5, v2
	v_med3_f32 v4, v4, s40, v213
	v_med3_f32 v2, v2, s40, v213
	v_cvt_pk_fp8_f32 v6, v4, v2 op_sel:[0,0,1]
	global_store_dword v[46:47], v9, off offset:48
	global_store_dword v[46:47], v6, off offset:56
	s_cbranch_scc0 .LBB0_656

; DI f32x16 mfma8(v8i a, v8i b, f32x16 c) { return __builtin_amdgcn_mfma_scale_f32_32x32x64_f8f6f4(a, b, c, 0, 0, 0, 0, 0, 0); }
; DI void attn_unit_d8(unsigned char* lds, const AttnArgs& a) {
;     ...
;     auto tile = [&](const unsigned char* Kb, const unsigned char* Kn, v8i& Pa, v8i& Pb, v8i& v0, v8i& v1, const v8i& Qa, const v8i& Qb, const v8i& w0, const v8i& w1) __attribute__((always_inline)) {
;         qk(Kb, 1, s1a, s1b);
;         v0 = rd32(Kb + voff); v1 = rd32(Kb + voff + 32 * A8_PITCH);
;         o0[0] = mfma8(w0, Qa, o0[0]); o1[0] = mfma8(w0, Qb, o1[0]); o0[1] = mfma8(w1, Qa, o0[1]); o1[1] = mfma8(w1, Qb, o1[1]);
;         expsum(s0a, l0); expsum(s0b, l1); pack4(s0a, Pa, 0); pack4(s0b, Pb, 0);
;         qk(Kn, 0, s0a, s0b);
;         expsum(s1a, l0); expsum(s1b, l1); pack4(s1a, Pa, 4); pack4(s1b, Pb, 4);
; #pragma unroll
;         for (int i = 0; i < 8; ++i) { __builtin_amdgcn_sched_group_barrier(0x008, 1, 0); __builtin_amdgcn_sched_group_barrier(0x402, 22, 0); }
;     };
;     for (int t = a.t0; t < a.t1; t += 2) {
;         const int s1 = sb + 1 >= 5 ? sb - 4 : sb + 1, s2 = sb + 2 >= 5 ? sb - 3 : sb + 2, s3 = sb + 3 >= 5 ? sb - 2 : sb + 3, s4 = sb + 4 >= 5 ? sb - 1 : sb + 4;
;         { const int ta = t + 3, tb = t + 4; gload(ta < a.t1 ? ta : a.t1 - 1, kreg0, vreg0); gload(tb < a.t1 ? tb : a.t1 - 1, kreg1, vreg1); }
;         tile(lds + sb * D8_SLOT, lds + s1 * D8_SLOT, PaX, PbX, vX0, vX1, PaY, PbY, vY0, vY1);
;         tile(lds + s1 * D8_SLOT, lds + s2 * D8_SLOT, PaY, PbY, vY0, vY1, PaX, PbX, vX0, vX1);
;         lstore(s3, kreg0, vreg0); lstore(s4, kreg1, vreg1);
;         __syncthreads();
;         sb = s2;
;     }
.LBB0_1888:
	s_add_i32 s22, s22, 2
	s_mul_i32 s8, s23, 0x2800
	s_cmp_gt_i32 s23, 3
	v_mfma_f32_32x32x64_f8f6f4 v[50:65], v[154:161], v[138:145], v[50:65]
	v_exp_f32_e32 v194, v90
	v_add_u32_e32 v90, s8, v219
	s_cselect_b32 s8, -4, 1
	s_add_i32 s51, s8, s23
	s_cmp_gt_i32 s23, 2
	s_cselect_b32 s8, -3, 2
	s_add_i32 s8, s8, s23
	s_cmp_gt_i32 s23, 1
	s_cselect_b32 s52, -2, 3
	s_add_i32 s52, s52, s23
	s_cmp_gt_i32 s23, 0
	s_cselect_b32 s53, -1, 4
	s_min_u32 s56, s22, 64
	s_add_i32 s53, s53, s23
	s_cmp_lt_u32 s22, 61
	s_mul_i32 s50, s8, 0x2800
	s_mov_b32 s23, s8
	s_cselect_b64 s[54:55], -1, 0
	s_lshl_b32 s8, s56, 6
	s_add_i32 s56, s8, 0xc0
	s_add_i32 s57, s8, 0xfffff0c0
	s_and_b64 s[54:55], s[54:55], exec
	v_lshl_add_u64 v[98:99], v[184:185], 0, s[8:9]
	s_cselect_b32 s8, s56, s57
	s_cselect_b32 s55, s19, s21
	s_cselect_b32 s54, s18, s20
	s_min_u32 s58, s22, 63
	v_exp_f32_e32 v200, v82
	v_exp_f32_e32 v201, v83
	v_exp_f32_e32 v198, v84
	v_exp_f32_e32 v199, v85
	v_exp_f32_e32 v202, v86
	v_exp_f32_e32 v203, v87
	v_exp_f32_e32 v196, v88
	v_exp_f32_e32 v197, v89
	ds_read_b128 v[82:85], v90 offset:2560
	ds_read_b128 v[86:89], v90 offset:2576
	global_load_dwordx2 v[204:205], v[98:99], off offset:192
	v_add_u32_e32 v98, s8, v182
	s_cmp_lt_u32 s22, 60
	v_ashrrev_i32_e32 v99, 31, v98
	s_cselect_b64 s[56:57], -1, 0
	s_lshl_b32 s8, s58, 6
	v_lshlrev_b64 v[98:99], 8, v[98:99]
	s_add_i32 s58, s8, 0x100
	s_add_i32 s59, s8, 0xfffff100
	v_lshl_add_u64 v[98:99], s[54:55], 0, v[98:99]
	s_and_b64 s[54:55], s[56:57], exec
	v_lshl_add_u64 v[100:101], v[184:185], 0, s[8:9]
	s_cselect_b32 s8, s58, s59
	v_lshl_add_u64 v[220:221], v[98:99], 0, v[178:179]
	v_add_u32_e32 v98, s8, v182
	v_ashrrev_i32_e32 v99, 31, v98
	s_cselect_b32 s55, s19, s21
	s_cselect_b32 s54, s18, s20
	v_lshlrev_b64 v[98:99], 8, v[98:99]
	v_lshl_add_u64 v[98:99], s[54:55], 0, v[98:99]
	global_load_dwordx2 v[206:207], v[100:101], off offset:256
	v_lshl_add_u64 v[222:223], v[98:99], 0, v[178:179]
	s_waitcnt lgkmcnt(0)
	v_mfma_f32_32x32x64_f8f6f4 v[98:113], v[82:89], v[114:121], 0
	v_exp_f32_e32 v195, v91
	v_exp_f32_e32 v224, v92
	v_exp_f32_e32 v225, v93
	v_exp_f32_e32 v226, v94
	v_exp_f32_e32 v227, v95
	v_exp_f32_e32 v228, v96
	v_exp_f32_e32 v229, v97
	ds_read_b128 v[170:173], v90 offset:5120
	ds_read_b128 v[174:177], v90 offset:5136
	ds_read_b128 v[162:165], v90 offset:7680
	ds_read_b128 v[166:169], v90 offset:7696
	v_pk_add_f32 v[90:91], v[188:189], v[200:201]
	v_pk_add_f32 v[92:93], v[186:187], v[198:199]
	v_pk_add_f32 v[90:91], v[202:203], v[90:91]
	v_pk_add_f32 v[92:93], v[196:197], v[92:93]
	v_pk_add_f32 v[90:91], v[194:195], v[90:91]
	v_pk_add_f32 v[92:93], v[224:225], v[92:93]
	v_exp_f32_e32 v66, v66
	v_exp_f32_e32 v67, v67
	v_exp_f32_e32 v68, v68
	v_exp_f32_e32 v69, v69
	v_exp_f32_e32 v70, v70
	v_exp_f32_e32 v71, v71
	v_exp_f32_e32 v72, v72
	v_pk_add_f32 v[230:231], v[228:229], v[92:93]
	v_pk_add_f32 v[232:233], v[226:227], v[90:91]
	v_mfma_f32_32x32x64_f8f6f4 v[82:97], v[82:89], v[122:129], 0
	v_exp_f32_e32 v73, v73
	v_exp_f32_e32 v74, v74
	v_exp_f32_e32 v75, v75
	v_exp_f32_e32 v76, v76
	v_exp_f32_e32 v77, v77
	v_exp_f32_e32 v78, v78
	v_exp_f32_e32 v79, v79
	v_exp_f32_e32 v80, v80
	v_exp_f32_e32 v81, v81
	v_pk_add_f32 v[188:189], v[192:193], v[66:67]
	v_pk_add_f32 v[190:191], v[190:191], v[68:69]
	s_nop 0
	v_pk_add_f32 v[188:189], v[70:71], v[188:189]
	v_pk_add_f32 v[190:191], v[72:73], v[190:191]
	s_nop 0
	v_cvt_scalef32_pk_fp8_f32 v186, v200, v201, s36
	v_pk_add_f32 v[188:189], v[74:75], v[188:189]
	v_pk_add_f32 v[190:191], v[76:77], v[190:191]
	v_cvt_scalef32_pk_fp8_f32 v187, v202, v203, s36
	v_cvt_scalef32_pk_fp8_f32 v186, v198, v199, s36 op_sel:[0,0,0,1]
	v_pk_add_f32 v[192:193], v[78:79], v[188:189]
	v_pk_add_f32 v[190:191], v[80:81], v[190:191]
	v_mfma_f32_32x32x64_f8f6f4 v[2:17], v[154:161], v[130:137], v[2:17]
	s_nop 0
	s_nop 0
	s_nop 0
	s_nop 0
	s_nop 0
	s_nop 0
	s_mulk_i32 s51, 0x2800
	v_cvt_scalef32_pk_fp8_f32 v188, v194, v195, s36
	v_cvt_scalef32_pk_fp8_f32 v189, v226, v227, s36
	v_cvt_scalef32_pk_fp8_f32 v154, v66, v67, s36
	v_cvt_scalef32_pk_fp8_f32 v155, v70, v71, s36
	v_cvt_scalef32_pk_fp8_f32 v156, v74, v75, s36
	v_cvt_scalef32_pk_fp8_f32 v157, v78, v79, s36
	v_cvt_scalef32_pk_fp8_f32 v187, v196, v197, s36 op_sel:[0,0,0,1]
	v_add_u32_e32 v234, s51, v219
	v_cvt_scalef32_pk_fp8_f32 v188, v224, v225, s36 op_sel:[0,0,0,1]
	v_cvt_scalef32_pk_fp8_f32 v189, v228, v229, s36 op_sel:[0,0,0,1]
	v_cvt_scalef32_pk_fp8_f32 v154, v68, v69, s36 op_sel:[0,0,0,1]
	v_cvt_scalef32_pk_fp8_f32 v155, v72, v73, s36 op_sel:[0,0,0,1]
	v_cvt_scalef32_pk_fp8_f32 v156, v76, v77, s36 op_sel:[0,0,0,1]
	v_cvt_scalef32_pk_fp8_f32 v157, v80, v81, s36 op_sel:[0,0,0,1]
	v_exp_f32_e32 v98, v98
	v_exp_f32_e32 v99, v99
	v_mfma_f32_32x32x64_f8f6f4 v[34:49], v[146:153], v[138:145], v[34:49]
	v_exp_f32_e32 v100, v100
	v_exp_f32_e32 v101, v101
	v_exp_f32_e32 v102, v102
	v_exp_f32_e32 v103, v103
	v_exp_f32_e32 v104, v104
	v_exp_f32_e32 v105, v105
	v_exp_f32_e32 v106, v106
	v_exp_f32_e32 v107, v107
	v_exp_f32_e32 v108, v108
	v_exp_f32_e32 v109, v109
	v_exp_f32_e32 v110, v110
	v_exp_f32_e32 v111, v111
	v_exp_f32_e32 v112, v112
	v_exp_f32_e32 v113, v113
	ds_read_b128 v[194:197], v234
	ds_read_b128 v[198:201], v234 offset:16
	v_pk_add_f32 v[66:67], v[232:233], v[98:99]
	v_pk_add_f32 v[68:69], v[230:231], v[100:101]
	v_pk_add_f32 v[66:67], v[102:103], v[66:67]
	v_pk_add_f32 v[68:69], v[104:105], v[68:69]
	v_pk_add_f32 v[66:67], v[106:107], v[66:67]
	v_pk_add_f32 v[68:69], v[108:109], v[68:69]
	v_pk_add_f32 v[140:141], v[110:111], v[66:67]
	v_pk_add_f32 v[138:139], v[112:113], v[68:69]
	v_mfma_f32_32x32x64_f8f6f4 v[18:33], v[146:153], v[130:137], v[18:33]
	v_exp_f32_e32 v82, v82
	v_exp_f32_e32 v83, v83
	v_exp_f32_e32 v84, v84
	v_exp_f32_e32 v85, v85
	v_exp_f32_e32 v86, v86
	v_exp_f32_e32 v87, v87
	v_exp_f32_e32 v88, v88
	v_exp_f32_e32 v89, v89
	v_exp_f32_e32 v90, v90
	v_exp_f32_e32 v91, v91
	v_exp_f32_e32 v92, v92
	v_exp_f32_e32 v93, v93
	v_exp_f32_e32 v94, v94
	v_exp_f32_e32 v95, v95
	v_exp_f32_e32 v96, v96
	v_exp_f32_e32 v97, v97
	v_pk_add_f32 v[66:67], v[192:193], v[82:83]
	v_pk_add_f32 v[68:69], v[190:191], v[84:85]
	v_pk_add_f32 v[66:67], v[86:87], v[66:67]
	v_pk_add_f32 v[68:69], v[88:89], v[68:69]
	v_pk_add_f32 v[130:131], v[90:91], v[66:67]
	v_pk_add_f32 v[132:133], v[92:93], v[68:69]
	s_waitcnt lgkmcnt(0)
; DI void attn_unit_a8(unsigned char* lds, const AttnArgs& a) {
;     ...
;     auto w_decode = [&](int j, const float*& src, unsigned char*& dst, int& ld, int& n0, int& k0, bool& gu) __attribute__((always_inline)) {
;         const int g = (j >> 2) * 512 + a.wl, e = g / 96, rr = g - e * 96; KParamsPtr kp = kparams();
;         if (rr < 64) { src = kp->w_gu + ((size_t)a.wli * NE + e) * (1024 * 2048); dst = kp->ws + WS_WGU + (size_t)a.wli * SZ_WGU + (size_t)e * 2048 * 1024; ld = 2048; n0 = (rr & 7) * 256; k0 = ((rr >> 3) * 4 + (j & 3)) * 32; gu = true; }
;         else { const int q = rr - 64; src = kp->w_dn + ((size_t)a.wli * NE + e) * (1024 * 1024); dst = kp->ws + WS_WDN + (size_t)a.wli * SZ_WDN + (size_t)e * 1024 * 1024; ld = 1024; n0 = (q & 3) * 256; k0 = ((q >> 2) * 4 + (j & 3)) * 32; gu = false; } };
;     auto w_issue = [&](int j) __attribute__((always_inline)) { const float* src; unsigned char* dst; int ld, n0, k0; bool gu; w_decode(j, src, dst, ld, n0, k0, gu);
;         const float* p = src + (size_t)(k0 + 4 * wid) * ld + n0 + wn4;
;         wq[0] = __builtin_nontemporal_load((const f32x4*)p); wq[1] = __builtin_nontemporal_load((const f32x4*)(p + ld));
;         wq[2] = __builtin_nontemporal_load((const f32x4*)(p + (size_t)2 * ld)); wq[3] = __builtin_nontemporal_load((const f32x4*)(p + (size_t)3 * ld)); };
;     auto w_cvt = [&]() __attribute__((always_inline)) { unsigned char* t8 = lds + AT_WT + wn4 * WPITCH + 4 * wid;
; #pragma unroll
; DI void attn_unit_d8(unsigned char* lds, const AttnArgs& a) {
;     ...
;     auto tile = [&](const unsigned char* Kb, const unsigned char* Kn, v8i& Pa, v8i& Pb, v8i& v0, v8i& v1, const v8i& Qa, const v8i& Qb, const v8i& w0, const v8i& w1) __attribute__((always_inline)) {
;         qk(Kb, 1, s1a, s1b);
;         v0 = rd32(Kb + voff); v1 = rd32(Kb + voff + 32 * A8_PITCH);
;         o0[0] = mfma8(w0, Qa, o0[0]); o1[0] = mfma8(w0, Qb, o1[0]); o0[1] = mfma8(w1, Qa, o0[1]); o1[1] = mfma8(w1, Qb, o1[1]);
;         expsum(s0a, l0); expsum(s0b, l1); pack4(s0a, Pa, 0); pack4(s0b, Pb, 0);
;         qk(Kn, 0, s0a, s0b);
;         expsum(s1a, l0); expsum(s1b, l1); pack4(s1a, Pa, 4); pack4(s1b, Pb, 4);
; #pragma unroll
;         for (int i = 0; i < 8; ++i) { __builtin_amdgcn_sched_group_barrier(0x008, 1, 0); __builtin_amdgcn_sched_group_barrier(0x402, 22, 0); }
;     };
	v_mfma_f32_32x32x64_f8f6f4 v[66:81], v[194:201], v[114:121], 0
	s_nop 0
	s_nop 0
	s_nop 0
	s_nop 0
	s_nop 0
	s_nop 0
	s_nop 0
	v_cvt_scalef32_pk_fp8_f32 v190, v98, v99, s36
	v_cvt_scalef32_pk_fp8_f32 v191, v102, v103, s36
	v_cvt_scalef32_pk_fp8_f32 v192, v106, v107, s36
	v_cvt_scalef32_pk_fp8_f32 v193, v110, v111, s36
	v_cvt_scalef32_pk_fp8_f32 v158, v82, v83, s36
	v_cvt_scalef32_pk_fp8_f32 v159, v86, v87, s36
	v_pk_add_f32 v[142:143], v[96:97], v[132:133]
	v_pk_add_f32 v[144:145], v[94:95], v[130:131]
	v_cvt_scalef32_pk_fp8_f32 v160, v90, v91, s36
	v_cvt_scalef32_pk_fp8_f32 v190, v100, v101, s36 op_sel:[0,0,0,1]
	v_cvt_scalef32_pk_fp8_f32 v191, v104, v105, s36 op_sel:[0,0,0,1]
	v_cvt_scalef32_pk_fp8_f32 v192, v108, v109, s36 op_sel:[0,0,0,1]
	v_cvt_scalef32_pk_fp8_f32 v193, v112, v113, s36 op_sel:[0,0,0,1]
	v_cvt_scalef32_pk_fp8_f32 v158, v84, v85, s36 op_sel:[0,0,0,1]
	v_cvt_scalef32_pk_fp8_f32 v159, v88, v89, s36 op_sel:[0,0,0,1]
	v_mfma_f32_32x32x64_f8f6f4 v[98:113], v[194:201], v[122:129], 0
	global_load_dwordx2 v[194:195], v[220:221], off
	global_load_dwordx2 v[196:197], v[222:223], off
	ds_read_b128 v[130:133], v234 offset:2560
	ds_read_b128 v[134:137], v234 offset:2576
	v_exp_f32_e32 v146, v66
	s_lshr_b32 s73, s61, 2
	v_exp_f32_e32 v147, v67
	s_lshl_b32 s73, s73, 9
	s_mulk_i32 s52, 0x2800
	s_nop 0
	s_add_i32 s8, s52, 0
	v_cvt_scalef32_pk_fp8_f32 v161, v94, v95, s36
	v_add_u32_e32 v224, s8, v183
	v_cvt_scalef32_pk_fp8_f32 v160, v92, v93, s36 op_sel:[0,0,0,1]
	v_cvt_scalef32_pk_fp8_f32 v161, v96, v97, s36 op_sel:[0,0,0,1]
	v_exp_f32_e32 v148, v68
	s_add_i32 s73, s73, s46
	v_exp_f32_e32 v149, v69
	s_mul_i32 s75, s73, 0xaaab
	v_exp_f32_e32 v150, v70
	s_lshr_b32 s75, s75, 22
	v_exp_f32_e32 v151, v71
	s_mul_i32 s76, s75, 0x60
	v_exp_f32_e32 v152, v72
	s_sub_i32 s76, s73, s76
	v_exp_f32_e32 v153, v73
	s_lshr_b32 s77, s76, 6
	v_exp_f32_e32 v198, v74
	s_lshl_b32 s78, s77, 6
	v_exp_f32_e32 v199, v75
	s_sub_i32 s76, s76, s78
	v_exp_f32_e32 v200, v76
	s_sub_i32 s78, 3, s77
	v_exp_f32_e32 v201, v77
	s_lshr_b32 s79, s76, s78
	v_exp_f32_e32 v202, v78
	s_lshl_b32 s79, s79, 2
	v_exp_f32_e32 v203, v79
	s_and_b32 s81, s61, 3
	v_exp_f32_e32 v220, v80
	s_add_i32 s79, s79, s81
	v_exp_f32_e32 v221, v81
	s_lshl_b32 s79, s79, 5
	v_pk_add_f32 v[66:67], v[140:141], v[146:147]
	s_waitcnt lgkmcnt(0)
	v_mfma_f32_32x32x64_f8f6f4 v[82:97], v[130:137], v[114:121], 0
	v_add_f32_e64 v68, v138, v148
	v_add_f32_e64 v69, v139, v149
	v_add_f32_e64 v66, v150, v66
	v_add_f32_e64 v67, v151, v67
	v_add_f32_e64 v68, v152, v68
	v_add_f32_e64 v69, v153, v69
	v_add_f32_e64 v138, v198, v66
	v_add_f32_e64 v139, v199, v67
	v_add_f32_e64 v140, v200, v68
	v_add_f32_e64 v141, v201, v69
	v_exp_f32_e32 v98, v98
	s_lshl_b32 s81, s63, 2
	v_exp_f32_e32 v99, v99
	s_add_i32 s81, s81, s79
	v_exp_f32_e32 v100, v100
	s_sub_i32 s78, 13, s77
	v_exp_f32_e32 v101, v101
	s_lshl_b32 s81, s81, s78
	v_exp_f32_e32 v102, v102
	s_lshr_b32 s78, 7, s77
	v_exp_f32_e32 v103, v103
	s_and_b32 s78, s76, s78
	v_exp_f32_e32 v104, v104
	s_lshl_b32 s72, s78, 10
	v_exp_f32_e32 v105, v105
	s_add_i32 s81, s81, s72
	v_exp_f32_e32 v106, v106
	s_add_i32 s72, s75, 32
	v_exp_f32_e32 v107, v107
	s_sub_i32 s80, 23, s77
	v_exp_f32_e32 v108, v108
	s_lshl_b32 s72, s72, s80
	v_exp_f32_e32 v109, v109
	s_add_i32 s81, s81, s72
	v_exp_f32_e32 v110, v110
	s_cmp_eq_u32 s77, 0
	s_cselect_b64 s[84:85], s[66:67], s[68:69]
	v_exp_f32_e32 v111, v111
	s_add_u32 s84, s84, s81
	s_addc_u32 s85, s85, 0
	v_exp_f32_e32 v112, v112
	s_lshr_b32 s80, 0x2000, s77
	v_exp_f32_e32 v113, v113
	s_and_b32 s72, s78, 3
	v_exp_f32_e32 v82, v82
	s_lshl_b32 s72, s72, 19
	v_mfma_f32_32x32x64_f8f6f4 v[66:81], v[130:137], v[122:129], 0
	v_add_f32_e64 v130, v144, v98
	v_add_f32_e64 v131, v145, v99
	v_add_f32_e64 v132, v142, v100
	v_add_f32_e64 v133, v143, v101
	v_add_f32_e64 v142, v102, v130
	v_add_f32_e64 v143, v103, v131
	v_add_f32_e64 v132, v104, v132
	v_add_f32_e64 v133, v105, v133
	v_add_f32_e64 v134, v220, v140
	v_add_f32_e64 v135, v221, v141
	v_add_f32_e64 v136, v202, v138
	v_add_f32_e64 v137, v203, v139
	s_nop 0
	s_nop 0
	s_nop 0
	s_nop 0
	s_nop 0
	s_nop 0
	v_pk_add_f32 v[142:143], v[106:107], v[142:143]
	v_pk_add_f32 v[132:133], v[108:109], v[132:133]
	v_cvt_scalef32_pk_fp8_f32 v138, v146, v147, s36
	v_cvt_scalef32_pk_fp8_f32 v139, v150, v151, s36
	v_cvt_scalef32_pk_fp8_f32 v140, v198, v199, s36
	v_cvt_scalef32_pk_fp8_f32 v141, v202, v203, s36
	v_cvt_scalef32_pk_fp8_f32 v130, v98, v99, s36
	v_cvt_scalef32_pk_fp8_f32 v131, v102, v103, s36
	v_pk_add_f32 v[146:147], v[112:113], v[132:133]
	v_pk_add_f32 v[150:151], v[110:111], v[142:143]
	v_mfma_f32_32x32x64_f8f6f4 v[50:65], v[170:177], v[186:193], v[50:65]
	v_exp_f32_e32 v83, v83
	s_lshr_b32 s81, s78, 2
	v_exp_f32_e32 v84, v84
	s_lshl_b32 s81, s81, 17
	v_exp_f32_e32 v85, v85
; DI unsigned pk4_fp8_mul64(float a, float b, float c, float d) { v2s_t r = {0, 0}; r = __builtin_amdgcn_cvt_scalef32_pk_fp8_f32(r, a, b, 0.015625f, false); r = __builtin_amdgcn_cvt_scalef32_pk_fp8_f32(r, c, d, 0.015625f, true); return __builtin_bit_cast(unsigned, r); }
; DI f32x16 mfma8(v8i a, v8i b, f32x16 c) { return __builtin_amdgcn_mfma_scale_f32_32x32x64_f8f6f4(a, b, c, 0, 0, 0, 0, 0, 0); }
; DI void attn_unit_a8(unsigned char* lds, const AttnArgs& a) {
;     ...
;     auto w_cvt = [&]() __attribute__((always_inline)) { unsigned char* t8 = lds + AT_WT + wn4 * WPITCH + 4 * wid;
; #pragma unroll
;         for (int j = 0; j < 4; ++j) *(unsigned*)(t8 + j * WPITCH) = pk4_fp8_mul64(wq[0][j], wq[1][j], wq[2][j], wq[3][j]); };
;     const int wcol = tid >> 1, whalf = tid & 1;
;     const unsigned wper_gu = (unsigned)((wcol >> 7) * 256 + (wcol & 96) + invperm32(wcol & 31)) * 1024u + 16u * whalf;
;     const unsigned wper_dn = (unsigned)fwd_lane16(wcol) * 1024u + 16u * whalf;
;     auto w_store = [&](int j) __attribute__((always_inline)) { const float* src; unsigned char* dst; int ld, n0, k0; bool gu; w_decode(j, src, dst, ld, n0, k0, gu);
;         const int nb = n0 >> 8; const unsigned uni = (unsigned)(gu ? (nb & 3) * 512 + (nb >> 2) * 128 : nb * 256) * 1024u + (unsigned)k0;
;         const unsigned off = (gu ? wper_gu : wper_dn) + uni;
;         const unsigned* t = (const unsigned*)(lds + AT_WT + wcol * WPITCH + 16 * whalf);
;         *(u32x4*)(dst + off) = (u32x4){t[0], t[1], t[2], t[3]}; };
; DI void attn_unit_d8(unsigned char* lds, const AttnArgs& a) {
;     ...
;     auto tile = [&](const unsigned char* Kb, const unsigned char* Kn, v8i& Pa, v8i& Pb, v8i& v0, v8i& v1, const v8i& Qa, const v8i& Qb, const v8i& w0, const v8i& w1) __attribute__((always_inline)) {
;         qk(Kb, 1, s1a, s1b);
;         v0 = rd32(Kb + voff); v1 = rd32(Kb + voff + 32 * A8_PITCH);
;         o0[0] = mfma8(w0, Qa, o0[0]); o1[0] = mfma8(w0, Qb, o1[0]); o0[1] = mfma8(w1, Qa, o0[1]); o1[1] = mfma8(w1, Qb, o1[1]);
;         expsum(s0a, l0); expsum(s0b, l1); pack4(s0a, Pa, 0); pack4(s0b, Pb, 0);
;         qk(Kn, 0, s0a, s0b);
;         expsum(s1a, l0); expsum(s1b, l1); pack4(s1a, Pa, 4); pack4(s1b, Pb, 4);
; #pragma unroll
;         for (int i = 0; i < 8; ++i) { __builtin_amdgcn_sched_group_barrier(0x008, 1, 0); __builtin_amdgcn_sched_group_barrier(0x402, 22, 0); }
;     };
	s_add_i32 s72, s72, s81
	v_add_u32_e32 v102, s50, v219
	v_exp_f32_e32 v86, v86
	s_lshl_b32 s81, s78, 18
	v_exp_f32_e32 v87, v87
	s_cmp_eq_u32 s77, 0
	s_cselect_b32 s72, s72, s81
	v_exp_f32_e32 v88, v88
	s_mul_i32 s81, s77, 0xc000000
	v_exp_f32_e32 v89, v89
	s_add_i32 s81, s81, 0x9094000
	v_cvt_scalef32_pk_fp8_f32 v130, v100, v101, s36 op_sel:[0,0,0,1]
	v_cvt_scalef32_pk_fp8_f32 v131, v104, v105, s36 op_sel:[0,0,0,1]
	v_exp_f32_e32 v90, v90
	s_add_i32 s72, s72, s79
	v_exp_f32_e32 v91, v91
	s_sub_i32 s73, 21, s77
	v_exp_f32_e32 v92, v92
	s_lshl_b32 s73, s75, s73
	v_exp_f32_e32 v93, v93
	s_add_i32 s72, s72, s73
	ds_read_b128 v[98:101], v102
	ds_read_b128 v[102:105], v102 offset:16
	s_nop 0
	v_cvt_scalef32_pk_fp8_f32 v138, v148, v149, s36 op_sel:[0,0,0,1]
	v_cvt_scalef32_pk_fp8_f32 v139, v152, v153, s36 op_sel:[0,0,0,1]
	v_cvt_scalef32_pk_fp8_f32 v140, v200, v201, s36 op_sel:[0,0,0,1]
	v_cvt_scalef32_pk_fp8_f32 v141, v220, v221, s36 op_sel:[0,0,0,1]
	s_nop 0
	v_exp_f32_e32 v94, v94
	s_add_u32 s72, s72, s81
	v_exp_f32_e32 v95, v95
	s_or_b32 s79, s72, s77
	v_mfma_f32_32x32x64_f8f6f4 v[2:17], v[170:177], v[154:161], v[2:17]
	v_exp_f32_e32 v148, v96
	v_cvt_scalef32_pk_fp8_f32 v132, v106, v107, s36
	v_exp_f32_e32 v149, v97
	v_pk_add_f32 v[96:97], v[136:137], v[82:83]
	v_pk_add_f32 v[106:107], v[134:135], v[84:85]
	v_exp_f32_e32 v66, v66
	v_exp_f32_e32 v67, v67
	v_exp_f32_e32 v68, v68
	v_exp_f32_e32 v69, v69
	v_cvt_scalef32_pk_fp8_f32 v133, v110, v111, s36
	v_pk_add_f32 v[106:107], v[88:89], v[106:107]
	v_pk_add_f32 v[96:97], v[86:87], v[96:97]
	v_exp_f32_e32 v70, v70
	v_exp_f32_e32 v71, v71
	v_exp_f32_e32 v72, v72
	v_exp_f32_e32 v73, v73
	v_cvt_scalef32_pk_fp8_f32 v132, v108, v109, s36 op_sel:[0,0,0,1]
	v_cvt_scalef32_pk_fp8_f32 v133, v112, v113, s36 op_sel:[0,0,0,1]
	v_pk_add_f32 v[96:97], v[90:91], v[96:97]
	v_pk_add_f32 v[106:107], v[92:93], v[106:107]
	v_exp_f32_e32 v74, v74
	v_exp_f32_e32 v75, v75
	v_mfma_f32_32x32x64_f8f6f4 v[34:49], v[162:169], v[186:193], v[34:49]
	v_exp_f32_e32 v76, v76
	v_exp_f32_e32 v77, v77
	v_exp_f32_e32 v78, v78
	v_exp_f32_e32 v79, v79
	s_nop 0
	v_exp_f32_e32 v80, v80
	v_exp_f32_e32 v81, v81
	s_nop 0
	s_nop 0
	v_cvt_scalef32_pk_fp8_f32 v142, v82, v83, s36
	s_nop 0
	v_cvt_scalef32_pk_fp8_f32 v143, v86, v87, s36
	v_cvt_scalef32_pk_fp8_f32 v144, v90, v91, s36
	v_cvt_scalef32_pk_fp8_f32 v142, v84, v85, s36 op_sel:[0,0,0,1]
	v_pk_add_f32 v[82:83], v[150:151], v[66:67]
	v_pk_add_f32 v[84:85], v[146:147], v[68:69]
	s_mulk_i32 s53, 0x2800
	v_pk_add_f32 v[186:187], v[148:149], v[106:107]
	v_pk_add_f32 v[188:189], v[94:95], v[96:97]
	v_cvt_scalef32_pk_fp8_f32 v145, v94, v95, s36
	v_cvt_scalef32_pk_fp8_f32 v143, v88, v89, s36 op_sel:[0,0,0,1]
	v_cvt_scalef32_pk_fp8_f32 v144, v92, v93, s36 op_sel:[0,0,0,1]
	v_pk_add_f32 v[84:85], v[72:73], v[84:85]
	v_mfma_f32_32x32x64_f8f6f4 v[18:33], v[162:169], v[154:161], v[18:33]
	v_add_f32_e64 v82, v70, v82
	v_add_f32_e64 v83, v71, v83
	s_nop 0
	s_nop 0
	s_nop 0
	s_nop 0
	s_add_i32 s51, s53, 0
	v_add_f32_e64 v82, v74, v82
	v_add_f32_e64 v83, v75, v83
	v_add_f32_e64 v84, v76, v84
	v_add_f32_e64 v85, v77, v85
	v_cvt_scalef32_pk_fp8_f32 v134, v66, v67, s36
	v_cvt_scalef32_pk_fp8_f32 v135, v70, v71, s36
	v_cvt_scalef32_pk_fp8_f32 v136, v74, v75, s36
	v_cvt_scalef32_pk_fp8_f32 v137, v78, v79, s36
	v_pk_add_f32 v[190:191], v[80:81], v[84:85]
	v_pk_add_f32 v[192:193], v[78:79], v[82:83]
	v_add_u32_e32 v106, s8, v218
	v_add_u32_e32 v107, s51, v183
	v_cvt_scalef32_pk_fp8_f32 v145, v148, v149, s36 op_sel:[0,0,0,1]
	v_cvt_scalef32_pk_fp8_f32 v134, v68, v69, s36 op_sel:[0,0,0,1]
	v_cvt_scalef32_pk_fp8_f32 v135, v72, v73, s36 op_sel:[0,0,0,1]
	v_cvt_scalef32_pk_fp8_f32 v136, v76, v77, s36 op_sel:[0,0,0,1]
	v_cvt_scalef32_pk_fp8_f32 v137, v80, v81, s36 op_sel:[0,0,0,1]
	s_waitcnt lgkmcnt(0)
	v_mfma_f32_32x32x64_f8f6f4 v[82:97], v[98:105], v[114:121], 0
	ds_read_b128 v[154:157], v234 offset:5120
	ds_read_b128 v[158:161], v234 offset:5136
	ds_read_b128 v[146:149], v234 offset:7680
	ds_read_b128 v[150:153], v234 offset:7696
	s_cmpk_gt_i32 s46, 0x1ff
	s_cbranch_scc1 .Lmy_rd1_ldum
	s_add_i32 s72, s61, -1
	s_cmp_lt_u32 s72, 24
	s_cbranch_scc0 .Lmy_rd1_noc
	s_waitcnt vmcnt(4)
	v_cvt_scalef32_pk_fp8_f32 v236, v236, v240, s62
	v_cvt_scalef32_pk_fp8_f32 v237, v237, v241, s62
	v_cvt_scalef32_pk_fp8_f32 v238, v238, v242, s62
	v_cvt_scalef32_pk_fp8_f32 v239, v239, v243, s62
	v_cvt_scalef32_pk_fp8_f32 v236, v244, v248, s62 op_sel:[0,0,0,1]
	v_cvt_scalef32_pk_fp8_f32 v237, v245, v249, s62 op_sel:[0,0,0,1]
	v_cvt_scalef32_pk_fp8_f32 v238, v246, v250, s62 op_sel:[0,0,0,1]
	v_cvt_scalef32_pk_fp8_f32 v239, v247, v251, s62 op_sel:[0,0,0,1]
	ds_write_b32 v252, v236
	ds_write_b32 v252, v237 offset:36
	ds_write_b32 v252, v238 offset:72
	ds_write_b32 v252, v239 offset:108

; DI unsigned pk4_fp8_mul64(float a, float b, float c, float d) { v2s_t r = {0, 0}; r = __builtin_amdgcn_cvt_scalef32_pk_fp8_f32(r, a, b, 0.015625f, false); r = __builtin_amdgcn_cvt_scalef32_pk_fp8_f32(r, c, d, 0.015625f, true); return __builtin_bit_cast(unsigned, r); }
; DI void attn_unit_a8(unsigned char* lds, const AttnArgs& a) {
;     ...
;     auto w_issue = [&](int j) __attribute__((always_inline)) { const float* src; unsigned char* dst; int ld, n0, k0; bool gu; w_decode(j, src, dst, ld, n0, k0, gu);
;         const float* p = src + (size_t)(k0 + 4 * wid) * ld + n0 + wn4;
;         wq[0] = __builtin_nontemporal_load((const f32x4*)p); wq[1] = __builtin_nontemporal_load((const f32x4*)(p + ld));
;         wq[2] = __builtin_nontemporal_load((const f32x4*)(p + (size_t)2 * ld)); wq[3] = __builtin_nontemporal_load((const f32x4*)(p + (size_t)3 * ld)); };
;     auto w_cvt = [&]() __attribute__((always_inline)) { unsigned char* t8 = lds + AT_WT + wn4 * WPITCH + 4 * wid;
; #pragma unroll
;         for (int j = 0; j < 4; ++j) *(unsigned*)(t8 + j * WPITCH) = pk4_fp8_mul64(wq[0][j], wq[1][j], wq[2][j], wq[3][j]); };
;     const int wcol = tid >> 1, whalf = tid & 1;
;     const unsigned wper_gu = (unsigned)((wcol >> 7) * 256 + (wcol & 96) + invperm32(wcol & 31)) * 1024u + 16u * whalf;
;     const unsigned wper_dn = (unsigned)fwd_lane16(wcol) * 1024u + 16u * whalf;
;     auto w_store = [&](int j) __attribute__((always_inline)) { const float* src; unsigned char* dst; int ld, n0, k0; bool gu; w_decode(j, src, dst, ld, n0, k0, gu);
;         const int nb = n0 >> 8; const unsigned uni = (unsigned)(gu ? (nb & 3) * 512 + (nb >> 2) * 128 : nb * 256) * 1024u + (unsigned)k0;
;         const unsigned off = (gu ? wper_gu : wper_dn) + uni;
;         const unsigned* t = (const unsigned*)(lds + AT_WT + wcol * WPITCH + 16 * whalf);
;         *(u32x4*)(dst + off) = (u32x4){t[0], t[1], t[2], t[3]}; };
.Lmy_rd1_lgo:
	global_load_dwordx4 v[236:239], v235, s[84:85] nt
	s_add_u32 s84, s84, s80
	s_addc_u32 s85, s85, 0
	global_load_dwordx4 v[240:243], v235, s[84:85] nt
	s_add_u32 s84, s84, s80
	s_addc_u32 s85, s85, 0
	s_cmpk_gt_i32 s46, 0x1ff
	s_cbranch_scc1 .Lmy_rd1_sdum
	s_add_i32 s72, s61, -2
	s_cmp_lt_u32 s72, 24
	s_cbranch_scc0 .Lmy_rd1_sdum
	s_andn2_b32 s73, s65, 1
	s_add_u32 s82, s70, s73
	s_addc_u32 s83, s71, 0
	s_bitcmp1_b32 s65, 0
	s_cbranch_scc1 .Lmy_rd1_sdn
	s_waitcnt lgkmcnt(0)
	global_store_dwordx4 v254, v[244:247], s[82:83]
	s_branch .Lmy_rd1_sdone

; DI f32x16 mfma8(v8i a, v8i b, f32x16 c) { return __builtin_amdgcn_mfma_scale_f32_32x32x64_f8f6f4(a, b, c, 0, 0, 0, 0, 0, 0); }
; DI void attn_unit_a8(unsigned char* lds, const AttnArgs& a) {
;     ...
;     auto w_issue = [&](int j) __attribute__((always_inline)) { const float* src; unsigned char* dst; int ld, n0, k0; bool gu; w_decode(j, src, dst, ld, n0, k0, gu);
;         const float* p = src + (size_t)(k0 + 4 * wid) * ld + n0 + wn4;
;         wq[0] = __builtin_nontemporal_load((const f32x4*)p); wq[1] = __builtin_nontemporal_load((const f32x4*)(p + ld));
;         wq[2] = __builtin_nontemporal_load((const f32x4*)(p + (size_t)2 * ld)); wq[3] = __builtin_nontemporal_load((const f32x4*)(p + (size_t)3 * ld)); };
; DI void attn_unit_d8(unsigned char* lds, const AttnArgs& a) {
;     ...
;         lstore(s3, kreg0, vreg0); lstore(s4, kreg1, vreg1);
;         __syncthreads();
;         sb = s2;
;     }
;     o0[0] = mfma8(vY0, PaY, o0[0]); o1[0] = mfma8(vY0, PbY, o1[0]); o0[1] = mfma8(vY1, PaY, o0[1]); o1[1] = mfma8(vY1, PbY, o1[1]);
;     __builtin_amdgcn_s_setprio(0);
;     float lt0 = l0[0] + l0[1] + l0[2] + l0[3]; lt0 += __shfl_xor(lt0, 32);
;     float lt1 = l1[0] + l1[1] + l1[2] + l1[3]; lt1 += __shfl_xor(lt1, 32);
;     unsigned char* op = a.out8 + (size_t)(wid * 32 + r) * 1024 + 4 * h;
;     const float r0 = 16.0f / lt0, r1 = 16.0f * a.lam / lt1;
;     float ss = 0.f;
; #pragma unroll
;     for (int d = 0; d < 2; ++d)
; #pragma unroll
;         for (int i = 0; i < 16; ++i) { const float v = o0[d][i] * r0 - o1[d][i] * r1; o0[d][i] = v; ss += v * v; }
;     ss += __shfl_xor(ss, 32);
;     const float rinv = rsqrtf(ss * (1.0f / 64.0f) + EPS) * a.oscale * CAT_SCALE;
.Lmy_rd1_sdone:
	s_nop 0
	global_load_dwordx4 v[244:247], v235, s[84:85] nt
	s_add_u32 s84, s84, s80
	s_addc_u32 s85, s85, 0
	global_load_dwordx4 v[248:251], v235, s[84:85] nt
	s_mov_b32 s65, s64
	s_mov_b32 s64, s79
	v_xor_b32_e32 v252, 0x4000, v252
	v_xor_b32_e32 v253, 0x4000, v253
	s_add_i32 s61, s61, 1
	s_cmpk_lt_u32 s22, 0x42
	s_waitcnt vmcnt(6)
	ds_write_b64 v224, v[194:195]
	v_mfma_f32_32x32x64_f8f6f4 v[66:81], v[98:105], v[122:129], 0
	v_add_u32_e32 v98, s51, v218
	v_add_u32_e32 v99, 0x1400, v106
	v_add_u32_e32 v98, 0x1400, v98
	ds_write2_b32 v99, v204, v205 offset1:8
	s_waitcnt vmcnt(5)
	ds_write_b64 v107, v[196:197]
	ds_write2_b32 v98, v206, v207 offset1:8
	s_waitcnt lgkmcnt(0)
	s_barrier
	s_cbranch_scc1 .LBB0_1888
	s_lshl_b64 s[16:17], s[16:17], 10
	s_add_u32 s8, s10, s16
	s_addc_u32 s17, s11, s17
	s_add_u32 s16, s8, s47
	v_mfma_f32_32x32x64_f8f6f4 v[50:65], v[154:161], v[138:145], v[50:65]
	s_addc_u32 s17, s17, 0
	v_mfma_f32_32x32x64_f8f6f4 v[2:17], v[154:161], v[130:137], v[2:17]
	v_mfma_f32_32x32x64_f8f6f4 v[34:49], v[146:153], v[138:145], v[34:49]
	v_mfma_f32_32x32x64_f8f6f4 v[18:33], v[146:153], v[130:137], v[18:33]
	s_setprio 0
	v_add_f32_e32 v66, v188, v189
	v_add_f32_e32 v66, v186, v66
	v_add_f32_e32 v66, v187, v66
	ds_bpermute_b32 v67, v1, v66
	v_add_f32_e32 v68, v192, v193
	v_add_f32_e32 v68, v190, v68
	v_add_f32_e32 v68, v191, v68
	ds_bpermute_b32 v69, v1, v68
	s_waitcnt lgkmcnt(1)
	v_add_f32_e32 v66, v66, v67
	v_div_scale_f32 v67, s[18:19], v66, v66, s36
	v_rcp_f32_e32 v70, v67
	s_waitcnt lgkmcnt(0)
	v_add_f32_e32 v68, v68, v69
	v_lshlrev_b32_e32 v178, 2, v217
	s_add_i32 s46, s46, s60
	v_fma_f32 v69, -v67, v70, 1.0
	v_fmac_f32_e32 v70, v69, v70
	v_div_scale_f32 v69, vcc, s36, v66, s36
	v_mul_f32_e32 v71, v69, v70
	v_fma_f32 v72, -v67, v71, v69
	v_fmac_f32_e32 v71, v72, v70
	v_fma_f32 v67, -v67, v71, v69
	v_div_scale_f32 v69, s[18:19], v68, v68, v214
	v_rcp_f32_e32 v72, v69
	v_div_fmas_f32 v67, v67, v70, v71
	v_div_fixup_f32 v66, v67, v66, s36
	s_cmpk_gt_i32 s46, 0x1ff
	v_fma_f32 v67, -v69, v72, 1.0
	v_fmac_f32_e32 v72, v67, v72
	v_div_scale_f32 v67, vcc, v214, v68, v214
	v_mul_f32_e32 v70, v67, v72
	v_fma_f32 v71, -v69, v70, v67
	v_fmac_f32_e32 v70, v71, v72
	v_fma_f32 v67, -v69, v70, v67
	v_div_fmas_f32 v67, v67, v72, v70
	v_div_fixup_f32 v68, v67, v68, v214
	v_mul_f32_e32 v2, v2, v68
	v_fma_f32 v50, v50, v66, -v2
	v_mul_f32_e32 v2, v3, v68
	v_fma_f32 v51, v51, v66, -v2
	v_mul_f32_e32 v67, v51, v51
	v_mul_f32_e32 v2, v4, v68
	v_fmac_f32_e32 v67, v50, v50
	v_fma_f32 v52, v52, v66, -v2
	v_mul_f32_e32 v2, v5, v68
	v_fmac_f32_e32 v67, v52, v52
	v_fma_f32 v53, v53, v66, -v2
	v_mul_f32_e32 v2, v6, v68
	v_fmac_f32_e32 v67, v53, v53
	v_fma_f32 v54, v54, v66, -v2
	v_mul_f32_e32 v2, v7, v68
	v_fmac_f32_e32 v67, v54, v54
	v_fma_f32 v55, v55, v66, -v2
	v_mul_f32_e32 v2, v8, v68
	v_fmac_f32_e32 v67, v55, v55
	v_fma_f32 v56, v56, v66, -v2
	v_mul_f32_e32 v2, v9, v68
	v_fmac_f32_e32 v67, v56, v56
	v_fma_f32 v57, v57, v66, -v2
	v_mul_f32_e32 v2, v10, v68
	v_fmac_f32_e32 v67, v57, v57
	v_fma_f32 v58, v58, v66, -v2
	v_mul_f32_e32 v2, v11, v68
	v_fmac_f32_e32 v67, v58, v58
	v_fma_f32 v59, v59, v66, -v2
	v_mul_f32_e32 v2, v12, v68
	v_fmac_f32_e32 v67, v59, v59
	v_fma_f32 v60, v60, v66, -v2
	v_mul_f32_e32 v2, v13, v68
	v_fmac_f32_e32 v67, v60, v60
	v_fma_f32 v61, v61, v66, -v2
	v_mul_f32_e32 v14, v14, v68
	v_fmac_f32_e32 v67, v61, v61
	v_fma_f32 v62, v62, v66, -v14
	v_mul_f32_e32 v14, v15, v68
	v_fmac_f32_e32 v67, v62, v62
	v_fma_f32 v63, v63, v66, -v14
	v_mul_f32_e32 v14, v16, v68
	v_lshlrev_b32_e32 v69, 4, v217
	v_fmac_f32_e32 v67, v63, v63
	v_fma_f32 v64, v64, v66, -v14
	v_mul_f32_e32 v14, v17, v68
	global_load_dwordx4 v[2:5], v69, s[12:13] offset:480
	global_load_dwordx4 v[6:9], v69, s[12:13] offset:288
	global_load_dwordx4 v[10:13], v69, s[12:13] offset:256
	v_fmac_f32_e32 v67, v64, v64
	v_fma_f32 v65, v65, v66, -v14
	v_mul_f32_e32 v14, v18, v68
	v_fmac_f32_e32 v67, v65, v65
	v_fma_f32 v70, v34, v66, -v14
	v_mul_f32_e32 v14, v19, v68
	v_fmac_f32_e32 v67, v70, v70
	v_fma_f32 v71, v35, v66, -v14
	v_mul_f32_e32 v14, v20, v68
	v_fmac_f32_e32 v67, v71, v71
	v_fma_f32 v72, v36, v66, -v14
	v_mul_f32_e32 v14, v21, v68
	v_fmac_f32_e32 v67, v72, v72
	v_fma_f32 v73, v37, v66, -v14
	v_mul_f32_e32 v14, v22, v68
	v_fmac_f32_e32 v67, v73, v73
	v_fma_f32 v74, v38, v66, -v14
	v_mul_f32_e32 v14, v23, v68
	v_fmac_f32_e32 v67, v74, v74
	v_fma_f32 v75, v39, v66, -v14
	v_fmac_f32_e32 v67, v75, v75
	v_pk_mul_f32 v[14:15], v[24:25], v[68:69] op_sel_hi:[1,0]
	v_pk_mul_f32 v[22:23], v[32:33], v[68:69] op_sel_hi:[1,0]
	v_pk_fma_f32 v[34:35], v[40:41], v[66:67], v[14:15] op_sel_hi:[1,0,1] neg_lo:[0,0,1] neg_hi:[0,0,1]
	s_nop 0
	v_pk_mul_f32 v[14:15], v[34:35], v[34:35]
	s_nop 0
	v_add_f32_e32 v14, v14, v67
	v_add_f32_e32 v20, v15, v14
	v_pk_mul_f32 v[14:15], v[26:27], v[68:69] op_sel_hi:[1,0]
	s_nop 0
	v_pk_fma_f32 v[36:37], v[42:43], v[66:67], v[14:15] op_sel_hi:[1,0,1] neg_lo:[0,0,1] neg_hi:[0,0,1]
	global_load_dwordx4 v[14:17], v69, s[12:13] offset:320
	v_pk_mul_f32 v[18:19], v[36:37], v[36:37]
	v_pk_fma_f32 v[42:43], v[48:49], v[66:67], v[22:23] op_sel_hi:[1,0,1] neg_lo:[0,0,1] neg_hi:[0,0,1]
	v_add_f32_e32 v18, v18, v20
	v_add_f32_e32 v20, v19, v18
	v_pk_mul_f32 v[18:19], v[28:29], v[68:69] op_sel_hi:[1,0]
	v_pk_mul_f32 v[22:23], v[42:43], v[42:43]
	v_pk_fma_f32 v[38:39], v[44:45], v[66:67], v[18:19] op_sel_hi:[1,0,1] neg_lo:[0,0,1] neg_hi:[0,0,1]
	s_nop 0
	v_pk_mul_f32 v[18:19], v[38:39], v[38:39]
	s_nop 0
	v_add_f32_e32 v18, v18, v20
	v_add_f32_e32 v20, v19, v18
	v_pk_mul_f32 v[18:19], v[30:31], v[68:69] op_sel_hi:[1,0]
	s_nop 0
	v_pk_fma_f32 v[40:41], v[46:47], v[66:67], v[18:19] op_sel_hi:[1,0,1] neg_lo:[0,0,1] neg_hi:[0,0,1]
	s_nop 0
	v_pk_mul_f32 v[18:19], v[40:41], v[40:41]
	s_nop 0
	v_add_f32_e32 v18, v18, v20
	v_add_f32_e32 v24, v19, v18
	v_add_f32_e32 v22, v22, v24
	v_add_f32_e32 v26, v23, v22
	ds_bpermute_b32 v27, v1, v26
	global_load_dwordx4 v[18:21], v69, s[12:13] offset:352
	global_load_dwordx4 v[22:25], v69, s[12:13] offset:448
	s_waitcnt lgkmcnt(0)
; DI unsigned pk4_fp8(float a, float b, float c, float d) { int r = 0; r = __builtin_amdgcn_cvt_pk_fp8_f32(a, b, r, false); r = __builtin_amdgcn_cvt_pk_fp8_f32(c, d, r, true); return (unsigned)r; }
; DI float clamp448(float x) { return __builtin_amdgcn_fmed3f(x, -448.0f, 448.0f); }
; DI void attn_unit_d8(unsigned char* lds, const AttnArgs& a) {
;     ...
;     const float r0 = 16.0f / lt0, r1 = 16.0f * a.lam / lt1;
;     float ss = 0.f;
; #pragma unroll
;     for (int d = 0; d < 2; ++d)
; #pragma unroll
;         for (int i = 0; i < 16; ++i) { const float v = o0[d][i] * r0 - o1[d][i] * r1; o0[d][i] = v; ss += v * v; }
;     ss += __shfl_xor(ss, 32);
;     const float rinv = rsqrtf(ss * (1.0f / 64.0f) + EPS) * a.oscale * CAT_SCALE;
;     f32x4 ggv[2][4];
; #pragma unroll
;     for (int d = 0; d < 2; ++d)
; #pragma unroll
;         for (int g = 0; g < 4; ++g) ggv[d][g] = *(const f32x4*)(a.subg + 32 * d + 8 * g + 4 * h);
;     asm volatile("" : "+v"(ggv[0][0]), "+v"(ggv[1][3]));
; #pragma unroll
;     for (int d = 0; d < 2; ++d)
; #pragma unroll
;         for (int g = 0; g < 4; ++g) { const f32x4 gg = ggv[d][g];
;             *(unsigned*)(op + 32 * d + 8 * g) = pk4_fp8(clamp448(o0[d][4 * g] * rinv * gg[0]), clamp448(o0[d][4 * g + 1] * rinv * gg[1]), clamp448(o0[d][4 * g + 2] * rinv * gg[2]), clamp448(o0[d][4 * g + 3] * rinv * gg[3])); }
	v_add_f32_e32 v26, v26, v27
	v_fmamk_f32 v26, v26, 0x3c800000, v215
	v_mul_f32_e32 v27, 0x4b800000, v26
	v_cmp_gt_f32_e32 vcc, s41, v26
	s_nop 1
	v_cndmask_b32_e32 v30, v26, v27, vcc
	global_load_dwordx4 v[26:29], v69, s[12:13] offset:384
	v_rsq_f32_e32 v32, v30
	v_lshlrev_b64 v[30:31], 10, v[180:181]
	v_lshl_add_u64 v[44:45], s[16:17], 0, v[30:31]
	v_lshl_add_u64 v[44:45], v[44:45], 0, v[178:179]
	v_mul_f32_e32 v30, 0x45800000, v32
	v_cndmask_b32_e32 v30, v32, v30, vcc
	v_mul_f32_e32 v48, v213, v30
	global_load_dwordx4 v[30:33], v69, s[12:13] offset:416
	v_mul_f32_e32 v48, 0x41800000, v48
	s_waitcnt vmcnt(5)
	v_mul_f32_e32 v49, v50, v48
	v_mul_f32_e32 v10, v10, v49
	v_mul_f32_e32 v49, v51, v48
	v_mul_f32_e32 v11, v11, v49
	v_mul_f32_e32 v49, v52, v48
	v_med3_f32 v10, v10, s42, v216
	v_med3_f32 v11, v11, s42, v216
	v_mul_f32_e32 v12, v12, v49
	s_nop 0
	v_cvt_pk_fp8_f32 v49, v10, v11
	v_mul_f32_e32 v10, v53, v48
	v_mul_f32_e32 v10, v13, v10
	v_med3_f32 v12, v12, s42, v216
	v_med3_f32 v10, v10, s42, v216
	v_cvt_pk_fp8_f32 v49, v12, v10 op_sel:[0,0,1]
	v_mul_f32_e32 v10, v54, v48
	v_mul_f32_e32 v6, v6, v10
	v_mul_f32_e32 v10, v55, v48
	v_mul_f32_e32 v7, v7, v10
	v_mul_f32_e32 v10, v56, v48
	v_med3_f32 v6, v6, s42, v216
	v_med3_f32 v7, v7, s42, v216
	v_mul_f32_e32 v8, v8, v10
	s_nop 0
	v_cvt_pk_fp8_f32 v10, v6, v7
	v_mul_f32_e32 v6, v57, v48
	v_mul_f32_e32 v6, v9, v6
	v_med3_f32 v8, v8, s42, v216
	v_med3_f32 v6, v6, s42, v216
	v_cvt_pk_fp8_f32 v10, v8, v6 op_sel:[0,0,1]
	v_add_co_u32_e32 v6, vcc, s43, v44
	v_lshl_add_u64 v[46:47], v[44:45], 0, s[14:15]
	s_nop 0
	v_addc_co_u32_e32 v7, vcc, 0, v45, vcc
	global_store_dword v[6:7], v49, off offset:768
	global_store_dword v[46:47], v10, off offset:8
	v_mul_f32_e32 v6, v58, v48
	v_mul_f32_e32 v7, v59, v48
	s_waitcnt vmcnt(6)
	v_mul_f32_e32 v6, v14, v6
	v_mul_f32_e32 v7, v15, v7
	v_med3_f32 v6, v6, s42, v216
	v_med3_f32 v7, v7, s42, v216
	s_nop 0
	v_cvt_pk_fp8_f32 v9, v6, v7
	v_mul_f32_e32 v8, v60, v48
	v_mul_f32_e32 v6, v61, v48
	v_mul_f32_e32 v8, v16, v8
	v_mul_f32_e32 v6, v17, v6
	v_med3_f32 v8, v8, s42, v216
	v_med3_f32 v6, v6, s42, v216
	v_cvt_pk_fp8_f32 v9, v8, v6 op_sel:[0,0,1]
	v_mul_f32_e32 v6, v62, v48
	v_mul_f32_e32 v7, v63, v48
	s_nop 0
	v_mul_f32_e32 v8, v64, v48
	s_nop 0
	s_waitcnt vmcnt(5)
	v_mul_f32_e32 v6, v18, v6
	v_mul_f32_e32 v7, v19, v7
	v_med3_f32 v6, v6, s42, v216
	v_med3_f32 v7, v7, s42, v216
	v_cvt_pk_fp8_f32 v10, v6, v7
	v_mul_f32_e32 v6, v65, v48
	v_mul_f32_e32 v8, v20, v8
	v_mul_f32_e32 v6, v21, v6
	v_med3_f32 v8, v8, s42, v216
	v_med3_f32 v6, v6, s42, v216
	v_cvt_pk_fp8_f32 v10, v8, v6 op_sel:[0,0,1]
	v_mul_f32_e32 v6, v70, v48
	v_mul_f32_e32 v7, v71, v48
	s_waitcnt vmcnt(3)
	v_mul_f32_e32 v6, v26, v6
	v_mul_f32_e32 v7, v27, v7
	v_med3_f32 v6, v6, s42, v216
	v_med3_f32 v7, v7, s42, v216
	v_cvt_pk_fp8_f32 v11, v6, v7
	v_mul_f32_e32 v8, v72, v48
	v_mul_f32_e32 v6, v73, v48
	v_mul_f32_e32 v8, v28, v8
	v_mul_f32_e32 v6, v29, v6
	v_med3_f32 v8, v8, s42, v216
	v_med3_f32 v6, v6, s42, v216
	v_cvt_pk_fp8_f32 v11, v8, v6 op_sel:[0,0,1]
	v_mul_f32_e32 v6, v74, v48
	v_mul_f32_e32 v7, v75, v48
	s_waitcnt vmcnt(2)
	v_mul_f32_e32 v6, v30, v6
	v_mul_f32_e32 v7, v31, v7
	v_med3_f32 v6, v6, s42, v216
	v_med3_f32 v7, v7, s42, v216
	s_nop 0
	v_cvt_pk_fp8_f32 v12, v6, v7
	v_mul_f32_e32 v8, v34, v48
	v_mul_f32_e32 v6, v35, v48
	v_mul_f32_e32 v8, v32, v8
	v_mul_f32_e32 v6, v33, v6
	v_med3_f32 v8, v8, s42, v216
	v_med3_f32 v6, v6, s42, v216
	v_cvt_pk_fp8_f32 v12, v8, v6 op_sel:[0,0,1]
	v_mul_f32_e32 v6, v36, v48
	v_mul_f32_e32 v7, v37, v48
	v_mul_f32_e32 v6, v22, v6
	v_mul_f32_e32 v7, v23, v7
	global_store_dword v[46:47], v9, off offset:16
	global_store_dword v[46:47], v10, off offset:24
	global_store_dword v[46:47], v11, off offset:32
	global_store_dword v[46:47], v12, off offset:40
	v_med3_f32 v6, v6, s42, v216
	v_med3_f32 v7, v7, s42, v216
	s_nop 0
	v_cvt_pk_fp8_f32 v9, v6, v7
	v_mul_f32_e32 v8, v38, v48
	v_mul_f32_e32 v6, v39, v48
	v_mul_f32_e32 v8, v24, v8
	v_mul_f32_e32 v6, v25, v6
	v_med3_f32 v8, v8, s42, v216
	v_med3_f32 v6, v6, s42, v216
	v_cvt_pk_fp8_f32 v9, v8, v6 op_sel:[0,0,1]
	v_mul_f32_e32 v6, v40, v48
	v_mul_f32_e32 v2, v2, v6
	v_mul_f32_e32 v6, v41, v48
	v_mul_f32_e32 v3, v3, v6
	v_mul_f32_e32 v6, v42, v48
	v_med3_f32 v2, v2, s42, v216
	v_med3_f32 v3, v3, s42, v216
	v_mul_f32_e32 v4, v4, v6
	s_nop 0
	v_cvt_pk_fp8_f32 v6, v2, v3
	v_mul_f32_e32 v2, v43, v48
	v_mul_f32_e32 v2, v5, v2
	v_med3_f32 v4, v4, s42, v216
	v_med3_f32 v2, v2, s42, v216
	v_cvt_pk_fp8_f32 v6, v4, v2 op_sel:[0,0,1]
	global_store_dword v[46:47], v9, off offset:48
	global_store_dword v[46:47], v6, off offset:56
	s_cbranch_scc0 .LBB0_1885
